# stack: conversion rewrite + scan QK pipelined LDS reads + adaLN GEMV deeper load pipelining + attention PV counted waits + conflict-free K swizzle
# speedup vs baseline: 1.0056x; 1.0056x over previous
.LBB0_16:
	s_nop 1
	v_readfirstlane_b32 s98, v4
	v_readfirstlane_b32 s99, v5
	v_lshlrev_b32_e32 v192, 2, v222
	s_sub_u32 s98, s98, 0x54000
	s_subb_u32 s99, s99, 0
	s_add_i32 s100, s11, 0x12000
	global_load_dword v80, v192, s[98:99]
	s_add_u32 s98, s98, 0xc000
	s_addc_u32 s99, s99, 0
	global_load_dword v81, v192, s[98:99]
	s_add_u32 s98, s98, 0xc000
	s_addc_u32 s99, s99, 0
	global_load_dword v82, v192, s[98:99]
	s_add_u32 s98, s98, 0xc000
	s_addc_u32 s99, s99, 0
	global_load_dword v83, v192, s[98:99]
	s_add_u32 s98, s98, 0xc000
	s_addc_u32 s99, s99, 0
	global_load_dword v84, v192, s[98:99]
	s_add_u32 s98, s98, 0xc000
	s_addc_u32 s99, s99, 0
	global_load_dword v85, v192, s[98:99]
	s_add_u32 s98, s98, 0xc000
	s_addc_u32 s99, s99, 0
	global_load_dword v86, v192, s[98:99]
	s_add_u32 s98, s98, 0xc000
	s_addc_u32 s99, s99, 0
	global_load_dword v87, v192, s[98:99]
	s_add_u32 s98, s98, 0xc000
	s_addc_u32 s99, s99, 0
	global_load_dword v88, v192, s[98:99]
	s_add_u32 s98, s98, 0xc000
	s_addc_u32 s99, s99, 0
	global_load_dword v89, v192, s[98:99]
	s_add_u32 s98, s98, 0xc000
	s_addc_u32 s99, s99, 0
	global_load_dword v90, v192, s[98:99]
	s_add_u32 s98, s98, 0xc000
	s_addc_u32 s99, s99, 0
	global_load_dword v91, v192, s[98:99]
	s_add_u32 s98, s98, 0xc000
	s_addc_u32 s99, s99, 0
	global_load_dword v92, v192, s[98:99]
	s_add_u32 s98, s98, 0xc000
	s_addc_u32 s99, s99, 0
	global_load_dword v93, v192, s[98:99]
	s_add_u32 s98, s98, 0xc000
	s_addc_u32 s99, s99, 0
	global_load_dword v94, v192, s[98:99]
	s_add_u32 s98, s98, 0xc000
	s_addc_u32 s99, s99, 0
	global_load_dword v95, v192, s[98:99]
	s_add_u32 s98, s98, 0xc000
	s_addc_u32 s99, s99, 0
	s_mov_b32 s101, 8
.Lgemv_a_loop:
	global_load_dword v96, v192, s[98:99]
	s_add_u32 s98, s98, 0xc000
	s_addc_u32 s99, s99, 0
	global_load_dword v97, v192, s[98:99]
	s_add_u32 s98, s98, 0xc000
	s_addc_u32 s99, s99, 0
	global_load_dword v98, v192, s[98:99]
	s_add_u32 s98, s98, 0xc000
	s_addc_u32 s99, s99, 0
	global_load_dword v99, v192, s[98:99]
	s_add_u32 s98, s98, 0xc000
	s_addc_u32 s99, s99, 0
	global_load_dword v100, v192, s[98:99]
	s_add_u32 s98, s98, 0xc000
	s_addc_u32 s99, s99, 0
	global_load_dword v101, v192, s[98:99]
	s_add_u32 s98, s98, 0xc000
	s_addc_u32 s99, s99, 0
	global_load_dword v102, v192, s[98:99]
	s_add_u32 s98, s98, 0xc000
	s_addc_u32 s99, s99, 0
	global_load_dword v103, v192, s[98:99]
	s_add_u32 s98, s98, 0xc000
	s_addc_u32 s99, s99, 0
	global_load_dword v104, v192, s[98:99]
	s_add_u32 s98, s98, 0xc000
	s_addc_u32 s99, s99, 0
	global_load_dword v105, v192, s[98:99]
	s_add_u32 s98, s98, 0xc000
	s_addc_u32 s99, s99, 0
	global_load_dword v106, v192, s[98:99]
	s_add_u32 s98, s98, 0xc000
	s_addc_u32 s99, s99, 0
	global_load_dword v107, v192, s[98:99]
	s_add_u32 s98, s98, 0xc000
	s_addc_u32 s99, s99, 0
	global_load_dword v108, v192, s[98:99]
	s_add_u32 s98, s98, 0xc000
	s_addc_u32 s99, s99, 0
	global_load_dword v109, v192, s[98:99]
	s_add_u32 s98, s98, 0xc000
	s_addc_u32 s99, s99, 0
	global_load_dword v110, v192, s[98:99]
	s_add_u32 s98, s98, 0xc000
	s_addc_u32 s99, s99, 0
	global_load_dword v111, v192, s[98:99]
	s_add_u32 s98, s98, 0xc000
	s_addc_u32 s99, s99, 0
	v_mov_b32_e32 v193, s100
	s_add_i32 s100, s100, 64
	ds_read_b128 v[112:115], v193
	ds_read_b128 v[116:119], v193 offset:16
	ds_read_b128 v[120:123], v193 offset:32
	ds_read_b128 v[124:127], v193 offset:48
	ds_read_b128 v[128:131], v193 offset:8192
	ds_read_b128 v[132:135], v193 offset:8208
	ds_read_b128 v[136:139], v193 offset:8224
	ds_read_b128 v[140:143], v193 offset:8240
	ds_read_b128 v[144:147], v193 offset:16384
	ds_read_b128 v[148:151], v193 offset:16400
	ds_read_b128 v[152:155], v193 offset:16416
	ds_read_b128 v[156:159], v193 offset:16432
	ds_read_b128 v[160:163], v193 offset:24576
	ds_read_b128 v[164:167], v193 offset:24592
	ds_read_b128 v[168:171], v193 offset:24608
	ds_read_b128 v[172:175], v193 offset:24624
	ds_read_b128 v[176:179], v193 offset:32768
	ds_read_b128 v[180:183], v193 offset:32784
	ds_read_b128 v[184:187], v193 offset:32800
	ds_read_b128 v[188:191], v193 offset:32816
	s_waitcnt vmcnt(16) lgkmcnt(0)
	v_fmac_f32_e32 v6, v80, v112
	v_fmac_f32_e32 v7, v80, v128
	v_fmac_f32_e32 v8, v80, v144
	v_fmac_f32_e32 v9, v80, v160
	v_fmac_f32_e32 v3, v80, v176
	v_fmac_f32_e32 v6, v81, v113
	v_fmac_f32_e32 v7, v81, v129
	v_fmac_f32_e32 v8, v81, v145
	v_fmac_f32_e32 v9, v81, v161
	v_fmac_f32_e32 v3, v81, v177
	v_fmac_f32_e32 v6, v82, v114
	v_fmac_f32_e32 v7, v82, v130
	v_fmac_f32_e32 v8, v82, v146
	v_fmac_f32_e32 v9, v82, v162
	v_fmac_f32_e32 v3, v82, v178
	v_fmac_f32_e32 v6, v83, v115
	v_fmac_f32_e32 v7, v83, v131
	v_fmac_f32_e32 v8, v83, v147
	v_fmac_f32_e32 v9, v83, v163
	v_fmac_f32_e32 v3, v83, v179
	v_fmac_f32_e32 v6, v84, v116
	v_fmac_f32_e32 v7, v84, v132
	v_fmac_f32_e32 v8, v84, v148
	v_fmac_f32_e32 v9, v84, v164
	v_fmac_f32_e32 v3, v84, v180
	v_fmac_f32_e32 v6, v85, v117
	v_fmac_f32_e32 v7, v85, v133
	v_fmac_f32_e32 v8, v85, v149
	v_fmac_f32_e32 v9, v85, v165
	v_fmac_f32_e32 v3, v85, v181
	v_fmac_f32_e32 v6, v86, v118
	v_fmac_f32_e32 v7, v86, v134
	v_fmac_f32_e32 v8, v86, v150
	v_fmac_f32_e32 v9, v86, v166
	v_fmac_f32_e32 v3, v86, v182
	v_fmac_f32_e32 v6, v87, v119
	v_fmac_f32_e32 v7, v87, v135
	v_fmac_f32_e32 v8, v87, v151
	v_fmac_f32_e32 v9, v87, v167
	v_fmac_f32_e32 v3, v87, v183
	v_fmac_f32_e32 v6, v88, v120
	v_fmac_f32_e32 v7, v88, v136
	v_fmac_f32_e32 v8, v88, v152
	v_fmac_f32_e32 v9, v88, v168
	v_fmac_f32_e32 v3, v88, v184
	v_fmac_f32_e32 v6, v89, v121
	v_fmac_f32_e32 v7, v89, v137
	v_fmac_f32_e32 v8, v89, v153
	v_fmac_f32_e32 v9, v89, v169
	v_fmac_f32_e32 v3, v89, v185
	v_fmac_f32_e32 v6, v90, v122
	v_fmac_f32_e32 v7, v90, v138
	v_fmac_f32_e32 v8, v90, v154
	v_fmac_f32_e32 v9, v90, v170
	v_fmac_f32_e32 v3, v90, v186
	v_fmac_f32_e32 v6, v91, v123
	v_fmac_f32_e32 v7, v91, v139
	v_fmac_f32_e32 v8, v91, v155
	v_fmac_f32_e32 v9, v91, v171
	v_fmac_f32_e32 v3, v91, v187
	v_fmac_f32_e32 v6, v92, v124
	v_fmac_f32_e32 v7, v92, v140
	v_fmac_f32_e32 v8, v92, v156
	v_fmac_f32_e32 v9, v92, v172
	v_fmac_f32_e32 v3, v92, v188
	v_fmac_f32_e32 v6, v93, v125
	v_fmac_f32_e32 v7, v93, v141
	v_fmac_f32_e32 v8, v93, v157
	v_fmac_f32_e32 v9, v93, v173
	v_fmac_f32_e32 v3, v93, v189
	v_fmac_f32_e32 v6, v94, v126
	v_fmac_f32_e32 v7, v94, v142
	v_fmac_f32_e32 v8, v94, v158
	v_fmac_f32_e32 v9, v94, v174
	v_fmac_f32_e32 v3, v94, v190
	v_fmac_f32_e32 v6, v95, v127
	v_fmac_f32_e32 v7, v95, v143
	v_fmac_f32_e32 v8, v95, v159
	v_fmac_f32_e32 v9, v95, v175
	v_fmac_f32_e32 v3, v95, v191
	s_cmp_eq_u32 s101, 1
	s_cbranch_scc1 .Lgemv_a_lastB
	global_load_dword v80, v192, s[98:99]
	s_add_u32 s98, s98, 0xc000
	s_addc_u32 s99, s99, 0
	global_load_dword v81, v192, s[98:99]
	s_add_u32 s98, s98, 0xc000
	s_addc_u32 s99, s99, 0
	global_load_dword v82, v192, s[98:99]
	s_add_u32 s98, s98, 0xc000
	s_addc_u32 s99, s99, 0
	global_load_dword v83, v192, s[98:99]
	s_add_u32 s98, s98, 0xc000
	s_addc_u32 s99, s99, 0
	global_load_dword v84, v192, s[98:99]
	s_add_u32 s98, s98, 0xc000
	s_addc_u32 s99, s99, 0
	global_load_dword v85, v192, s[98:99]
	s_add_u32 s98, s98, 0xc000
	s_addc_u32 s99, s99, 0
	global_load_dword v86, v192, s[98:99]
	s_add_u32 s98, s98, 0xc000
	s_addc_u32 s99, s99, 0
	global_load_dword v87, v192, s[98:99]
	s_add_u32 s98, s98, 0xc000
	s_addc_u32 s99, s99, 0
	global_load_dword v88, v192, s[98:99]
	s_add_u32 s98, s98, 0xc000
	s_addc_u32 s99, s99, 0
	global_load_dword v89, v192, s[98:99]
	s_add_u32 s98, s98, 0xc000
	s_addc_u32 s99, s99, 0
	global_load_dword v90, v192, s[98:99]
	s_add_u32 s98, s98, 0xc000
	s_addc_u32 s99, s99, 0
	global_load_dword v91, v192, s[98:99]
	s_add_u32 s98, s98, 0xc000
	s_addc_u32 s99, s99, 0
	global_load_dword v92, v192, s[98:99]
	s_add_u32 s98, s98, 0xc000
	s_addc_u32 s99, s99, 0
	global_load_dword v93, v192, s[98:99]
	s_add_u32 s98, s98, 0xc000
	s_addc_u32 s99, s99, 0
	global_load_dword v94, v192, s[98:99]
	s_add_u32 s98, s98, 0xc000
	s_addc_u32 s99, s99, 0
	global_load_dword v95, v192, s[98:99]
	s_add_u32 s98, s98, 0xc000
	s_addc_u32 s99, s99, 0
	v_mov_b32_e32 v193, s100
	s_add_i32 s100, s100, 64
	ds_read_b128 v[112:115], v193
	ds_read_b128 v[116:119], v193 offset:16
	ds_read_b128 v[120:123], v193 offset:32
	ds_read_b128 v[124:127], v193 offset:48
	ds_read_b128 v[128:131], v193 offset:8192
	ds_read_b128 v[132:135], v193 offset:8208
	ds_read_b128 v[136:139], v193 offset:8224
	ds_read_b128 v[140:143], v193 offset:8240
	ds_read_b128 v[144:147], v193 offset:16384
	ds_read_b128 v[148:151], v193 offset:16400
	ds_read_b128 v[152:155], v193 offset:16416
	ds_read_b128 v[156:159], v193 offset:16432
	ds_read_b128 v[160:163], v193 offset:24576
	ds_read_b128 v[164:167], v193 offset:24592
	ds_read_b128 v[168:171], v193 offset:24608
	ds_read_b128 v[172:175], v193 offset:24624
	ds_read_b128 v[176:179], v193 offset:32768
	ds_read_b128 v[180:183], v193 offset:32784
	ds_read_b128 v[184:187], v193 offset:32800
	ds_read_b128 v[188:191], v193 offset:32816
	s_waitcnt vmcnt(16) lgkmcnt(0)
	v_fmac_f32_e32 v6, v96, v112
	v_fmac_f32_e32 v7, v96, v128
	v_fmac_f32_e32 v8, v96, v144
	v_fmac_f32_e32 v9, v96, v160
	v_fmac_f32_e32 v3, v96, v176
	v_fmac_f32_e32 v6, v97, v113
	v_fmac_f32_e32 v7, v97, v129
	v_fmac_f32_e32 v8, v97, v145
	v_fmac_f32_e32 v9, v97, v161
	v_fmac_f32_e32 v3, v97, v177
	v_fmac_f32_e32 v6, v98, v114
	v_fmac_f32_e32 v7, v98, v130
	v_fmac_f32_e32 v8, v98, v146
	v_fmac_f32_e32 v9, v98, v162
	v_fmac_f32_e32 v3, v98, v178
	v_fmac_f32_e32 v6, v99, v115
	v_fmac_f32_e32 v7, v99, v131
	v_fmac_f32_e32 v8, v99, v147
	v_fmac_f32_e32 v9, v99, v163
	v_fmac_f32_e32 v3, v99, v179
	v_fmac_f32_e32 v6, v100, v116
	v_fmac_f32_e32 v7, v100, v132
	v_fmac_f32_e32 v8, v100, v148
	v_fmac_f32_e32 v9, v100, v164
	v_fmac_f32_e32 v3, v100, v180
	v_fmac_f32_e32 v6, v101, v117
	v_fmac_f32_e32 v7, v101, v133
	v_fmac_f32_e32 v8, v101, v149
	v_fmac_f32_e32 v9, v101, v165
	v_fmac_f32_e32 v3, v101, v181
	v_fmac_f32_e32 v6, v102, v118
	v_fmac_f32_e32 v7, v102, v134
	v_fmac_f32_e32 v8, v102, v150
	v_fmac_f32_e32 v9, v102, v166
	v_fmac_f32_e32 v3, v102, v182
	v_fmac_f32_e32 v6, v103, v119
	v_fmac_f32_e32 v7, v103, v135
	v_fmac_f32_e32 v8, v103, v151
	v_fmac_f32_e32 v9, v103, v167
	v_fmac_f32_e32 v3, v103, v183
	v_fmac_f32_e32 v6, v104, v120
	v_fmac_f32_e32 v7, v104, v136
	v_fmac_f32_e32 v8, v104, v152
	v_fmac_f32_e32 v9, v104, v168
	v_fmac_f32_e32 v3, v104, v184
	v_fmac_f32_e32 v6, v105, v121
	v_fmac_f32_e32 v7, v105, v137
	v_fmac_f32_e32 v8, v105, v153
	v_fmac_f32_e32 v9, v105, v169
	v_fmac_f32_e32 v3, v105, v185
	v_fmac_f32_e32 v6, v106, v122
	v_fmac_f32_e32 v7, v106, v138
	v_fmac_f32_e32 v8, v106, v154
	v_fmac_f32_e32 v9, v106, v170
	v_fmac_f32_e32 v3, v106, v186
	v_fmac_f32_e32 v6, v107, v123
	v_fmac_f32_e32 v7, v107, v139
	v_fmac_f32_e32 v8, v107, v155
	v_fmac_f32_e32 v9, v107, v171
	v_fmac_f32_e32 v3, v107, v187
	v_fmac_f32_e32 v6, v108, v124
	v_fmac_f32_e32 v7, v108, v140
	v_fmac_f32_e32 v8, v108, v156
	v_fmac_f32_e32 v9, v108, v172
	v_fmac_f32_e32 v3, v108, v188
	v_fmac_f32_e32 v6, v109, v125
	v_fmac_f32_e32 v7, v109, v141
	v_fmac_f32_e32 v8, v109, v157
	v_fmac_f32_e32 v9, v109, v173
	v_fmac_f32_e32 v3, v109, v189
	v_fmac_f32_e32 v6, v110, v126
	v_fmac_f32_e32 v7, v110, v142
	v_fmac_f32_e32 v8, v110, v158
	v_fmac_f32_e32 v9, v110, v174
	v_fmac_f32_e32 v3, v110, v190
	v_fmac_f32_e32 v6, v111, v127
	v_fmac_f32_e32 v7, v111, v143
	v_fmac_f32_e32 v8, v111, v159
	v_fmac_f32_e32 v9, v111, v175
	v_fmac_f32_e32 v3, v111, v191
	s_sub_i32 s101, s101, 1
	s_branch .Lgemv_a_loop
.Lgemv_a_lastB:
	v_mov_b32_e32 v193, s100
	s_add_i32 s100, s100, 64
	ds_read_b128 v[112:115], v193
	ds_read_b128 v[116:119], v193 offset:16
	ds_read_b128 v[120:123], v193 offset:32
	ds_read_b128 v[124:127], v193 offset:48
	ds_read_b128 v[128:131], v193 offset:8192
	ds_read_b128 v[132:135], v193 offset:8208
	ds_read_b128 v[136:139], v193 offset:8224
	ds_read_b128 v[140:143], v193 offset:8240
	ds_read_b128 v[144:147], v193 offset:16384
	ds_read_b128 v[148:151], v193 offset:16400
	ds_read_b128 v[152:155], v193 offset:16416
	ds_read_b128 v[156:159], v193 offset:16432
	ds_read_b128 v[160:163], v193 offset:24576
	ds_read_b128 v[164:167], v193 offset:24592
	ds_read_b128 v[168:171], v193 offset:24608
	ds_read_b128 v[172:175], v193 offset:24624
	ds_read_b128 v[176:179], v193 offset:32768
	ds_read_b128 v[180:183], v193 offset:32784
	ds_read_b128 v[184:187], v193 offset:32800
	ds_read_b128 v[188:191], v193 offset:32816
	s_waitcnt vmcnt(0) lgkmcnt(0)
	v_fmac_f32_e32 v6, v96, v112
	v_fmac_f32_e32 v7, v96, v128
	v_fmac_f32_e32 v8, v96, v144
	v_fmac_f32_e32 v9, v96, v160
	v_fmac_f32_e32 v3, v96, v176
	v_fmac_f32_e32 v6, v97, v113
	v_fmac_f32_e32 v7, v97, v129
	v_fmac_f32_e32 v8, v97, v145
	v_fmac_f32_e32 v9, v97, v161
	v_fmac_f32_e32 v3, v97, v177
	v_fmac_f32_e32 v6, v98, v114
	v_fmac_f32_e32 v7, v98, v130
	v_fmac_f32_e32 v8, v98, v146
	v_fmac_f32_e32 v9, v98, v162
	v_fmac_f32_e32 v3, v98, v178
	v_fmac_f32_e32 v6, v99, v115
	v_fmac_f32_e32 v7, v99, v131
	v_fmac_f32_e32 v8, v99, v147
	v_fmac_f32_e32 v9, v99, v163
	v_fmac_f32_e32 v3, v99, v179
	v_fmac_f32_e32 v6, v100, v116
	v_fmac_f32_e32 v7, v100, v132
	v_fmac_f32_e32 v8, v100, v148
	v_fmac_f32_e32 v9, v100, v164
	v_fmac_f32_e32 v3, v100, v180
	v_fmac_f32_e32 v6, v101, v117
	v_fmac_f32_e32 v7, v101, v133
	v_fmac_f32_e32 v8, v101, v149
	v_fmac_f32_e32 v9, v101, v165
	v_fmac_f32_e32 v3, v101, v181
	v_fmac_f32_e32 v6, v102, v118
	v_fmac_f32_e32 v7, v102, v134
	v_fmac_f32_e32 v8, v102, v150
	v_fmac_f32_e32 v9, v102, v166
	v_fmac_f32_e32 v3, v102, v182
	v_fmac_f32_e32 v6, v103, v119
	v_fmac_f32_e32 v7, v103, v135
	v_fmac_f32_e32 v8, v103, v151
	v_fmac_f32_e32 v9, v103, v167
	v_fmac_f32_e32 v3, v103, v183
	v_fmac_f32_e32 v6, v104, v120
	v_fmac_f32_e32 v7, v104, v136
	v_fmac_f32_e32 v8, v104, v152
	v_fmac_f32_e32 v9, v104, v168
	v_fmac_f32_e32 v3, v104, v184
	v_fmac_f32_e32 v6, v105, v121
	v_fmac_f32_e32 v7, v105, v137
	v_fmac_f32_e32 v8, v105, v153
	v_fmac_f32_e32 v9, v105, v169
	v_fmac_f32_e32 v3, v105, v185
	v_fmac_f32_e32 v6, v106, v122
	v_fmac_f32_e32 v7, v106, v138
	v_fmac_f32_e32 v8, v106, v154
	v_fmac_f32_e32 v9, v106, v170
	v_fmac_f32_e32 v3, v106, v186
	v_fmac_f32_e32 v6, v107, v123
	v_fmac_f32_e32 v7, v107, v139
	v_fmac_f32_e32 v8, v107, v155
	v_fmac_f32_e32 v9, v107, v171
	v_fmac_f32_e32 v3, v107, v187
	v_fmac_f32_e32 v6, v108, v124
	v_fmac_f32_e32 v7, v108, v140
	v_fmac_f32_e32 v8, v108, v156
	v_fmac_f32_e32 v9, v108, v172
	v_fmac_f32_e32 v3, v108, v188
	v_fmac_f32_e32 v6, v109, v125
	v_fmac_f32_e32 v7, v109, v141
	v_fmac_f32_e32 v8, v109, v157
	v_fmac_f32_e32 v9, v109, v173
	v_fmac_f32_e32 v3, v109, v189
	v_fmac_f32_e32 v6, v110, v126
	v_fmac_f32_e32 v7, v110, v142
	v_fmac_f32_e32 v8, v110, v158
	v_fmac_f32_e32 v9, v110, v174
	v_fmac_f32_e32 v3, v110, v190
	v_fmac_f32_e32 v6, v111, v127
	v_fmac_f32_e32 v7, v111, v143
	v_fmac_f32_e32 v8, v111, v159
	v_fmac_f32_e32 v9, v111, v175
	v_fmac_f32_e32 v3, v111, v191
	s_mov_b32 s14, 0
	ds_write2st64_b32 v1, v6, v7 offset1:1
	ds_write2st64_b32 v1, v8, v9 offset0:2 offset1:3
	ds_write_b32 v1, v3 offset:1024

.LBB0_22:
	s_nop 1
	v_readfirstlane_b32 s98, v6
	v_readfirstlane_b32 s99, v7
	v_lshlrev_b32_e32 v192, 2, v222
	s_sub_u32 s98, s98, 0x54000
	s_subb_u32 s99, s99, 0
	s_add_i32 s100, s15, 0x12000
	global_load_dword v80, v192, s[98:99]
	s_add_u32 s98, s98, 0xc000
	s_addc_u32 s99, s99, 0
	global_load_dword v81, v192, s[98:99]
	s_add_u32 s98, s98, 0xc000
	s_addc_u32 s99, s99, 0
	global_load_dword v82, v192, s[98:99]
	s_add_u32 s98, s98, 0xc000
	s_addc_u32 s99, s99, 0
	global_load_dword v83, v192, s[98:99]
	s_add_u32 s98, s98, 0xc000
	s_addc_u32 s99, s99, 0
	global_load_dword v84, v192, s[98:99]
	s_add_u32 s98, s98, 0xc000
	s_addc_u32 s99, s99, 0
	global_load_dword v85, v192, s[98:99]
	s_add_u32 s98, s98, 0xc000
	s_addc_u32 s99, s99, 0
	global_load_dword v86, v192, s[98:99]
	s_add_u32 s98, s98, 0xc000
	s_addc_u32 s99, s99, 0
	global_load_dword v87, v192, s[98:99]
	s_add_u32 s98, s98, 0xc000
	s_addc_u32 s99, s99, 0
	global_load_dword v88, v192, s[98:99]
	s_add_u32 s98, s98, 0xc000
	s_addc_u32 s99, s99, 0
	global_load_dword v89, v192, s[98:99]
	s_add_u32 s98, s98, 0xc000
	s_addc_u32 s99, s99, 0
	global_load_dword v90, v192, s[98:99]
	s_add_u32 s98, s98, 0xc000
	s_addc_u32 s99, s99, 0
	global_load_dword v91, v192, s[98:99]
	s_add_u32 s98, s98, 0xc000
	s_addc_u32 s99, s99, 0
	global_load_dword v92, v192, s[98:99]
	s_add_u32 s98, s98, 0xc000
	s_addc_u32 s99, s99, 0
	global_load_dword v93, v192, s[98:99]
	s_add_u32 s98, s98, 0xc000
	s_addc_u32 s99, s99, 0
	global_load_dword v94, v192, s[98:99]
	s_add_u32 s98, s98, 0xc000
	s_addc_u32 s99, s99, 0
	global_load_dword v95, v192, s[98:99]
	s_add_u32 s98, s98, 0xc000
	s_addc_u32 s99, s99, 0
	s_mov_b32 s101, 8
.Lgemv_b_loop:
	global_load_dword v96, v192, s[98:99]
	s_add_u32 s98, s98, 0xc000
	s_addc_u32 s99, s99, 0
	global_load_dword v97, v192, s[98:99]
	s_add_u32 s98, s98, 0xc000
	s_addc_u32 s99, s99, 0
	global_load_dword v98, v192, s[98:99]
	s_add_u32 s98, s98, 0xc000
	s_addc_u32 s99, s99, 0
	global_load_dword v99, v192, s[98:99]
	s_add_u32 s98, s98, 0xc000
	s_addc_u32 s99, s99, 0
	global_load_dword v100, v192, s[98:99]
	s_add_u32 s98, s98, 0xc000
	s_addc_u32 s99, s99, 0
	global_load_dword v101, v192, s[98:99]
	s_add_u32 s98, s98, 0xc000
	s_addc_u32 s99, s99, 0
	global_load_dword v102, v192, s[98:99]
	s_add_u32 s98, s98, 0xc000
	s_addc_u32 s99, s99, 0
	global_load_dword v103, v192, s[98:99]
	s_add_u32 s98, s98, 0xc000
	s_addc_u32 s99, s99, 0
	global_load_dword v104, v192, s[98:99]
	s_add_u32 s98, s98, 0xc000
	s_addc_u32 s99, s99, 0
	global_load_dword v105, v192, s[98:99]
	s_add_u32 s98, s98, 0xc000
	s_addc_u32 s99, s99, 0
	global_load_dword v106, v192, s[98:99]
	s_add_u32 s98, s98, 0xc000
	s_addc_u32 s99, s99, 0
	global_load_dword v107, v192, s[98:99]
	s_add_u32 s98, s98, 0xc000
	s_addc_u32 s99, s99, 0
	global_load_dword v108, v192, s[98:99]
	s_add_u32 s98, s98, 0xc000
	s_addc_u32 s99, s99, 0
	global_load_dword v109, v192, s[98:99]
	s_add_u32 s98, s98, 0xc000
	s_addc_u32 s99, s99, 0
	global_load_dword v110, v192, s[98:99]
	s_add_u32 s98, s98, 0xc000
	s_addc_u32 s99, s99, 0
	global_load_dword v111, v192, s[98:99]
	s_add_u32 s98, s98, 0xc000
	s_addc_u32 s99, s99, 0
	v_mov_b32_e32 v193, s100
	s_add_i32 s100, s100, 64
	ds_read_b128 v[112:115], v193
	ds_read_b128 v[116:119], v193 offset:16
	ds_read_b128 v[120:123], v193 offset:32
	ds_read_b128 v[124:127], v193 offset:48
	ds_read_b128 v[128:131], v193 offset:8192
	ds_read_b128 v[132:135], v193 offset:8208
	ds_read_b128 v[136:139], v193 offset:8224
	ds_read_b128 v[140:143], v193 offset:8240
	ds_read_b128 v[144:147], v193 offset:16384
	ds_read_b128 v[148:151], v193 offset:16400
	ds_read_b128 v[152:155], v193 offset:16416
	ds_read_b128 v[156:159], v193 offset:16432
	ds_read_b128 v[160:163], v193 offset:24576
	ds_read_b128 v[164:167], v193 offset:24592
	ds_read_b128 v[168:171], v193 offset:24608
	ds_read_b128 v[172:175], v193 offset:24624
	ds_read_b128 v[176:179], v193 offset:32768
	ds_read_b128 v[180:183], v193 offset:32784
	ds_read_b128 v[184:187], v193 offset:32800
	ds_read_b128 v[188:191], v193 offset:32816
	s_waitcnt vmcnt(16) lgkmcnt(0)
	v_fmac_f32_e32 v8, v80, v112
	v_fmac_f32_e32 v9, v80, v128
	v_fmac_f32_e32 v10, v80, v144
	v_fmac_f32_e32 v11, v80, v160
	v_fmac_f32_e32 v5, v80, v176
	v_fmac_f32_e32 v8, v81, v113
	v_fmac_f32_e32 v9, v81, v129
	v_fmac_f32_e32 v10, v81, v145
	v_fmac_f32_e32 v11, v81, v161
	v_fmac_f32_e32 v5, v81, v177
	v_fmac_f32_e32 v8, v82, v114
	v_fmac_f32_e32 v9, v82, v130
	v_fmac_f32_e32 v10, v82, v146
	v_fmac_f32_e32 v11, v82, v162
	v_fmac_f32_e32 v5, v82, v178
	v_fmac_f32_e32 v8, v83, v115
	v_fmac_f32_e32 v9, v83, v131
	v_fmac_f32_e32 v10, v83, v147
	v_fmac_f32_e32 v11, v83, v163
	v_fmac_f32_e32 v5, v83, v179
	v_fmac_f32_e32 v8, v84, v116
	v_fmac_f32_e32 v9, v84, v132
	v_fmac_f32_e32 v10, v84, v148
	v_fmac_f32_e32 v11, v84, v164
	v_fmac_f32_e32 v5, v84, v180
	v_fmac_f32_e32 v8, v85, v117
	v_fmac_f32_e32 v9, v85, v133
	v_fmac_f32_e32 v10, v85, v149
	v_fmac_f32_e32 v11, v85, v165
	v_fmac_f32_e32 v5, v85, v181
	v_fmac_f32_e32 v8, v86, v118
	v_fmac_f32_e32 v9, v86, v134
	v_fmac_f32_e32 v10, v86, v150
	v_fmac_f32_e32 v11, v86, v166
	v_fmac_f32_e32 v5, v86, v182
	v_fmac_f32_e32 v8, v87, v119
	v_fmac_f32_e32 v9, v87, v135
	v_fmac_f32_e32 v10, v87, v151
	v_fmac_f32_e32 v11, v87, v167
	v_fmac_f32_e32 v5, v87, v183
	v_fmac_f32_e32 v8, v88, v120
	v_fmac_f32_e32 v9, v88, v136
	v_fmac_f32_e32 v10, v88, v152
	v_fmac_f32_e32 v11, v88, v168
	v_fmac_f32_e32 v5, v88, v184
	v_fmac_f32_e32 v8, v89, v121
	v_fmac_f32_e32 v9, v89, v137
	v_fmac_f32_e32 v10, v89, v153
	v_fmac_f32_e32 v11, v89, v169
	v_fmac_f32_e32 v5, v89, v185
	v_fmac_f32_e32 v8, v90, v122
	v_fmac_f32_e32 v9, v90, v138
	v_fmac_f32_e32 v10, v90, v154
	v_fmac_f32_e32 v11, v90, v170
	v_fmac_f32_e32 v5, v90, v186
	v_fmac_f32_e32 v8, v91, v123
	v_fmac_f32_e32 v9, v91, v139
	v_fmac_f32_e32 v10, v91, v155
	v_fmac_f32_e32 v11, v91, v171
	v_fmac_f32_e32 v5, v91, v187
	v_fmac_f32_e32 v8, v92, v124
	v_fmac_f32_e32 v9, v92, v140
	v_fmac_f32_e32 v10, v92, v156
	v_fmac_f32_e32 v11, v92, v172
	v_fmac_f32_e32 v5, v92, v188
	v_fmac_f32_e32 v8, v93, v125
	v_fmac_f32_e32 v9, v93, v141
	v_fmac_f32_e32 v10, v93, v157
	v_fmac_f32_e32 v11, v93, v173
	v_fmac_f32_e32 v5, v93, v189
	v_fmac_f32_e32 v8, v94, v126
	v_fmac_f32_e32 v9, v94, v142
	v_fmac_f32_e32 v10, v94, v158
	v_fmac_f32_e32 v11, v94, v174
	v_fmac_f32_e32 v5, v94, v190
	v_fmac_f32_e32 v8, v95, v127
	v_fmac_f32_e32 v9, v95, v143
	v_fmac_f32_e32 v10, v95, v159
	v_fmac_f32_e32 v11, v95, v175
	v_fmac_f32_e32 v5, v95, v191
	s_cmp_eq_u32 s101, 1
	s_cbranch_scc1 .Lgemv_b_lastB
	global_load_dword v80, v192, s[98:99]
	s_add_u32 s98, s98, 0xc000
	s_addc_u32 s99, s99, 0
	global_load_dword v81, v192, s[98:99]
	s_add_u32 s98, s98, 0xc000
	s_addc_u32 s99, s99, 0
	global_load_dword v82, v192, s[98:99]
	s_add_u32 s98, s98, 0xc000
	s_addc_u32 s99, s99, 0
	global_load_dword v83, v192, s[98:99]
	s_add_u32 s98, s98, 0xc000
	s_addc_u32 s99, s99, 0
	global_load_dword v84, v192, s[98:99]
	s_add_u32 s98, s98, 0xc000
	s_addc_u32 s99, s99, 0
	global_load_dword v85, v192, s[98:99]
	s_add_u32 s98, s98, 0xc000
	s_addc_u32 s99, s99, 0
	global_load_dword v86, v192, s[98:99]
	s_add_u32 s98, s98, 0xc000
	s_addc_u32 s99, s99, 0
	global_load_dword v87, v192, s[98:99]
	s_add_u32 s98, s98, 0xc000
	s_addc_u32 s99, s99, 0
	global_load_dword v88, v192, s[98:99]
	s_add_u32 s98, s98, 0xc000
	s_addc_u32 s99, s99, 0
	global_load_dword v89, v192, s[98:99]
	s_add_u32 s98, s98, 0xc000
	s_addc_u32 s99, s99, 0
	global_load_dword v90, v192, s[98:99]
	s_add_u32 s98, s98, 0xc000
	s_addc_u32 s99, s99, 0
	global_load_dword v91, v192, s[98:99]
	s_add_u32 s98, s98, 0xc000
	s_addc_u32 s99, s99, 0
	global_load_dword v92, v192, s[98:99]
	s_add_u32 s98, s98, 0xc000
	s_addc_u32 s99, s99, 0
	global_load_dword v93, v192, s[98:99]
	s_add_u32 s98, s98, 0xc000
	s_addc_u32 s99, s99, 0
	global_load_dword v94, v192, s[98:99]
	s_add_u32 s98, s98, 0xc000
	s_addc_u32 s99, s99, 0
	global_load_dword v95, v192, s[98:99]
	s_add_u32 s98, s98, 0xc000
	s_addc_u32 s99, s99, 0
	v_mov_b32_e32 v193, s100
	s_add_i32 s100, s100, 64
	ds_read_b128 v[112:115], v193
	ds_read_b128 v[116:119], v193 offset:16
	ds_read_b128 v[120:123], v193 offset:32
	ds_read_b128 v[124:127], v193 offset:48
	ds_read_b128 v[128:131], v193 offset:8192
	ds_read_b128 v[132:135], v193 offset:8208
	ds_read_b128 v[136:139], v193 offset:8224
	ds_read_b128 v[140:143], v193 offset:8240
	ds_read_b128 v[144:147], v193 offset:16384
	ds_read_b128 v[148:151], v193 offset:16400
	ds_read_b128 v[152:155], v193 offset:16416
	ds_read_b128 v[156:159], v193 offset:16432
	ds_read_b128 v[160:163], v193 offset:24576
	ds_read_b128 v[164:167], v193 offset:24592
	ds_read_b128 v[168:171], v193 offset:24608
	ds_read_b128 v[172:175], v193 offset:24624
	ds_read_b128 v[176:179], v193 offset:32768
	ds_read_b128 v[180:183], v193 offset:32784
	ds_read_b128 v[184:187], v193 offset:32800
	ds_read_b128 v[188:191], v193 offset:32816
	s_waitcnt vmcnt(16) lgkmcnt(0)
	v_fmac_f32_e32 v8, v96, v112
	v_fmac_f32_e32 v9, v96, v128
	v_fmac_f32_e32 v10, v96, v144
	v_fmac_f32_e32 v11, v96, v160
	v_fmac_f32_e32 v5, v96, v176
	v_fmac_f32_e32 v8, v97, v113
	v_fmac_f32_e32 v9, v97, v129
	v_fmac_f32_e32 v10, v97, v145
	v_fmac_f32_e32 v11, v97, v161
	v_fmac_f32_e32 v5, v97, v177
	v_fmac_f32_e32 v8, v98, v114
	v_fmac_f32_e32 v9, v98, v130
	v_fmac_f32_e32 v10, v98, v146
	v_fmac_f32_e32 v11, v98, v162
	v_fmac_f32_e32 v5, v98, v178
	v_fmac_f32_e32 v8, v99, v115
	v_fmac_f32_e32 v9, v99, v131
	v_fmac_f32_e32 v10, v99, v147
	v_fmac_f32_e32 v11, v99, v163
	v_fmac_f32_e32 v5, v99, v179
	v_fmac_f32_e32 v8, v100, v116
	v_fmac_f32_e32 v9, v100, v132
	v_fmac_f32_e32 v10, v100, v148
	v_fmac_f32_e32 v11, v100, v164
	v_fmac_f32_e32 v5, v100, v180
	v_fmac_f32_e32 v8, v101, v117
	v_fmac_f32_e32 v9, v101, v133
	v_fmac_f32_e32 v10, v101, v149
	v_fmac_f32_e32 v11, v101, v165
	v_fmac_f32_e32 v5, v101, v181
	v_fmac_f32_e32 v8, v102, v118
	v_fmac_f32_e32 v9, v102, v134
	v_fmac_f32_e32 v10, v102, v150
	v_fmac_f32_e32 v11, v102, v166
	v_fmac_f32_e32 v5, v102, v182
	v_fmac_f32_e32 v8, v103, v119
	v_fmac_f32_e32 v9, v103, v135
	v_fmac_f32_e32 v10, v103, v151
	v_fmac_f32_e32 v11, v103, v167
	v_fmac_f32_e32 v5, v103, v183
	v_fmac_f32_e32 v8, v104, v120
	v_fmac_f32_e32 v9, v104, v136
	v_fmac_f32_e32 v10, v104, v152
	v_fmac_f32_e32 v11, v104, v168
	v_fmac_f32_e32 v5, v104, v184
	v_fmac_f32_e32 v8, v105, v121
	v_fmac_f32_e32 v9, v105, v137
	v_fmac_f32_e32 v10, v105, v153
	v_fmac_f32_e32 v11, v105, v169
	v_fmac_f32_e32 v5, v105, v185
	v_fmac_f32_e32 v8, v106, v122
	v_fmac_f32_e32 v9, v106, v138
	v_fmac_f32_e32 v10, v106, v154
	v_fmac_f32_e32 v11, v106, v170
	v_fmac_f32_e32 v5, v106, v186
	v_fmac_f32_e32 v8, v107, v123
	v_fmac_f32_e32 v9, v107, v139
	v_fmac_f32_e32 v10, v107, v155
	v_fmac_f32_e32 v11, v107, v171
	v_fmac_f32_e32 v5, v107, v187
	v_fmac_f32_e32 v8, v108, v124
	v_fmac_f32_e32 v9, v108, v140
	v_fmac_f32_e32 v10, v108, v156
	v_fmac_f32_e32 v11, v108, v172
	v_fmac_f32_e32 v5, v108, v188
	v_fmac_f32_e32 v8, v109, v125
	v_fmac_f32_e32 v9, v109, v141
	v_fmac_f32_e32 v10, v109, v157
	v_fmac_f32_e32 v11, v109, v173
	v_fmac_f32_e32 v5, v109, v189
	v_fmac_f32_e32 v8, v110, v126
	v_fmac_f32_e32 v9, v110, v142
	v_fmac_f32_e32 v10, v110, v158
	v_fmac_f32_e32 v11, v110, v174
	v_fmac_f32_e32 v5, v110, v190
	v_fmac_f32_e32 v8, v111, v127
	v_fmac_f32_e32 v9, v111, v143
	v_fmac_f32_e32 v10, v111, v159
	v_fmac_f32_e32 v11, v111, v175
	v_fmac_f32_e32 v5, v111, v191
	s_sub_i32 s101, s101, 1
	s_branch .Lgemv_b_loop
.Lgemv_b_lastB:
	v_mov_b32_e32 v193, s100
	s_add_i32 s100, s100, 64
	ds_read_b128 v[112:115], v193
	ds_read_b128 v[116:119], v193 offset:16
	ds_read_b128 v[120:123], v193 offset:32
	ds_read_b128 v[124:127], v193 offset:48
	ds_read_b128 v[128:131], v193 offset:8192
	ds_read_b128 v[132:135], v193 offset:8208
	ds_read_b128 v[136:139], v193 offset:8224
	ds_read_b128 v[140:143], v193 offset:8240
	ds_read_b128 v[144:147], v193 offset:16384
	ds_read_b128 v[148:151], v193 offset:16400
	ds_read_b128 v[152:155], v193 offset:16416
	ds_read_b128 v[156:159], v193 offset:16432
	ds_read_b128 v[160:163], v193 offset:24576
	ds_read_b128 v[164:167], v193 offset:24592
	ds_read_b128 v[168:171], v193 offset:24608
	ds_read_b128 v[172:175], v193 offset:24624
	ds_read_b128 v[176:179], v193 offset:32768
	ds_read_b128 v[180:183], v193 offset:32784
	ds_read_b128 v[184:187], v193 offset:32800
	ds_read_b128 v[188:191], v193 offset:32816
	s_waitcnt vmcnt(0) lgkmcnt(0)
	v_fmac_f32_e32 v8, v96, v112
	v_fmac_f32_e32 v9, v96, v128
	v_fmac_f32_e32 v10, v96, v144
	v_fmac_f32_e32 v11, v96, v160
	v_fmac_f32_e32 v5, v96, v176
	v_fmac_f32_e32 v8, v97, v113
	v_fmac_f32_e32 v9, v97, v129
	v_fmac_f32_e32 v10, v97, v145
	v_fmac_f32_e32 v11, v97, v161
	v_fmac_f32_e32 v5, v97, v177
	v_fmac_f32_e32 v8, v98, v114
	v_fmac_f32_e32 v9, v98, v130
	v_fmac_f32_e32 v10, v98, v146
	v_fmac_f32_e32 v11, v98, v162
	v_fmac_f32_e32 v5, v98, v178
	v_fmac_f32_e32 v8, v99, v115
	v_fmac_f32_e32 v9, v99, v131
	v_fmac_f32_e32 v10, v99, v147
	v_fmac_f32_e32 v11, v99, v163
	v_fmac_f32_e32 v5, v99, v179
	v_fmac_f32_e32 v8, v100, v116
	v_fmac_f32_e32 v9, v100, v132
	v_fmac_f32_e32 v10, v100, v148
	v_fmac_f32_e32 v11, v100, v164
	v_fmac_f32_e32 v5, v100, v180
	v_fmac_f32_e32 v8, v101, v117
	v_fmac_f32_e32 v9, v101, v133
	v_fmac_f32_e32 v10, v101, v149
	v_fmac_f32_e32 v11, v101, v165
	v_fmac_f32_e32 v5, v101, v181
	v_fmac_f32_e32 v8, v102, v118
	v_fmac_f32_e32 v9, v102, v134
	v_fmac_f32_e32 v10, v102, v150
	v_fmac_f32_e32 v11, v102, v166
	v_fmac_f32_e32 v5, v102, v182
	v_fmac_f32_e32 v8, v103, v119
	v_fmac_f32_e32 v9, v103, v135
	v_fmac_f32_e32 v10, v103, v151
	v_fmac_f32_e32 v11, v103, v167
	v_fmac_f32_e32 v5, v103, v183
	v_fmac_f32_e32 v8, v104, v120
	v_fmac_f32_e32 v9, v104, v136
	v_fmac_f32_e32 v10, v104, v152
	v_fmac_f32_e32 v11, v104, v168
	v_fmac_f32_e32 v5, v104, v184
	v_fmac_f32_e32 v8, v105, v121
	v_fmac_f32_e32 v9, v105, v137
	v_fmac_f32_e32 v10, v105, v153
	v_fmac_f32_e32 v11, v105, v169
	v_fmac_f32_e32 v5, v105, v185
	v_fmac_f32_e32 v8, v106, v122
	v_fmac_f32_e32 v9, v106, v138
	v_fmac_f32_e32 v10, v106, v154
	v_fmac_f32_e32 v11, v106, v170
	v_fmac_f32_e32 v5, v106, v186
	v_fmac_f32_e32 v8, v107, v123
	v_fmac_f32_e32 v9, v107, v139
	v_fmac_f32_e32 v10, v107, v155
	v_fmac_f32_e32 v11, v107, v171
	v_fmac_f32_e32 v5, v107, v187
	v_fmac_f32_e32 v8, v108, v124
	v_fmac_f32_e32 v9, v108, v140
	v_fmac_f32_e32 v10, v108, v156
	v_fmac_f32_e32 v11, v108, v172
	v_fmac_f32_e32 v5, v108, v188
	v_fmac_f32_e32 v8, v109, v125
	v_fmac_f32_e32 v9, v109, v141
	v_fmac_f32_e32 v10, v109, v157
	v_fmac_f32_e32 v11, v109, v173
	v_fmac_f32_e32 v5, v109, v189
	v_fmac_f32_e32 v8, v110, v126
	v_fmac_f32_e32 v9, v110, v142
	v_fmac_f32_e32 v10, v110, v158
	v_fmac_f32_e32 v11, v110, v174
	v_fmac_f32_e32 v5, v110, v190
	v_fmac_f32_e32 v8, v111, v127
	v_fmac_f32_e32 v9, v111, v143
	v_fmac_f32_e32 v10, v111, v159
	v_fmac_f32_e32 v11, v111, v175
	v_fmac_f32_e32 v5, v111, v191
	s_mov_b32 s16, 0
	ds_write2st64_b32 v1, v8, v9 offset1:1
	ds_write2st64_b32 v1, v10, v11 offset0:2 offset1:3
	ds_write_b32 v1, v5 offset:1024

.LBB0_427:
	s_or_b64 exec, exec, s[28:29]
	v_lshl_add_u32 v182, v130, 2, s60
	ds_read_b32 v183, v182 offset:256
	s_and_b64 vcc, exec, s[58:59]
	s_cbranch_vccnz .Lqk_11
	s_and_b64 vcc, exec, s[54:55]
	s_cbranch_vccnz .Lqk_10
	v_mov_b32_e32 v94, v107
	v_mov_b32_e32 v95, v107
	v_mov_b32_e32 v96, v107
	v_mov_b32_e32 v97, v107
	v_mov_b32_e32 v98, v107
	v_mov_b32_e32 v99, v107
	v_mov_b32_e32 v100, v107
	v_mov_b32_e32 v101, v107
	s_branch .Lqk_done
.Lqk_10:
	ds_read_b128 v[102:105], v149
	ds_read_b128 v[184:187], v150 offset:33792
	ds_read_b128 v[188:191], v149 offset:64
	ds_read_b128 v[192:195], v150 offset:33856
	ds_read_b128 v[200:203], v149 offset:128
	ds_read_b128 v[204:207], v150 offset:33920
	ds_read_b128 v[208:211], v149 offset:192
	ds_read_b128 v[212:215], v150 offset:33984
	s_waitcnt lgkmcnt(6)
	v_mfma_f32_16x16x32_bf16 v[98:101], v[184:187], v[102:105], 0
	ds_read_b128 v[102:105], v149 offset:256
	ds_read_b128 v[184:187], v150 offset:34048
	s_waitcnt lgkmcnt(6)
	v_mfma_f32_16x16x32_bf16 v[98:101], v[192:195], v[188:191], v[98:101]
	ds_read_b128 v[188:191], v149 offset:320
	ds_read_b128 v[192:195], v150 offset:34112
	s_waitcnt lgkmcnt(6)
	v_mfma_f32_16x16x32_bf16 v[98:101], v[204:207], v[200:203], v[98:101]
	ds_read_b128 v[200:203], v149 offset:384
	ds_read_b128 v[204:207], v150 offset:34176
	s_waitcnt lgkmcnt(6)
	v_mfma_f32_16x16x32_bf16 v[98:101], v[212:215], v[208:211], v[98:101]
	ds_read_b128 v[208:211], v149 offset:448
	ds_read_b128 v[212:215], v150 offset:34240
	s_waitcnt lgkmcnt(6)
	v_mfma_f32_16x16x32_bf16 v[98:101], v[184:187], v[102:105], v[98:101]
	s_waitcnt lgkmcnt(4)
	v_mfma_f32_16x16x32_bf16 v[98:101], v[192:195], v[188:191], v[98:101]
	s_waitcnt lgkmcnt(2)
	v_mfma_f32_16x16x32_bf16 v[98:101], v[204:207], v[200:203], v[98:101]
	s_waitcnt lgkmcnt(0)
	v_mfma_f32_16x16x32_bf16 v[98:101], v[212:215], v[208:211], v[98:101]
	v_mov_b32_e32 v94, v107
	v_mov_b32_e32 v95, v107
	v_mov_b32_e32 v96, v107
	v_mov_b32_e32 v97, v107
	s_branch .Lqk_done
.Lqk_11:
	ds_read_b128 v[102:105], v149
	ds_read_b128 v[184:187], v150 offset:33792
	ds_read_b128 v[188:191], v150 offset:42240
	ds_read_b128 v[192:195], v149 offset:64
	ds_read_b128 v[200:203], v150 offset:33856
	ds_read_b128 v[204:207], v150 offset:42304
	ds_read_b128 v[208:211], v149 offset:128
	ds_read_b128 v[212:215], v150 offset:33920
	ds_read_b128 v[216:219], v150 offset:42368
	ds_read_b128 v[224:227], v149 offset:192
	ds_read_b128 v[228:231], v150 offset:33984
	ds_read_b128 v[232:235], v150 offset:42432
	s_waitcnt lgkmcnt(9)
	v_mfma_f32_16x16x32_bf16 v[98:101], v[184:187], v[102:105], 0
	v_mfma_f32_16x16x32_bf16 v[94:97], v[188:191], v[102:105], 0
	ds_read_b128 v[102:105], v149 offset:256
	ds_read_b128 v[184:187], v150 offset:34048
	ds_read_b128 v[188:191], v150 offset:42496
	s_waitcnt lgkmcnt(9)
	v_mfma_f32_16x16x32_bf16 v[98:101], v[200:203], v[192:195], v[98:101]
	v_mfma_f32_16x16x32_bf16 v[94:97], v[204:207], v[192:195], v[94:97]
	ds_read_b128 v[192:195], v149 offset:320
	ds_read_b128 v[200:203], v150 offset:34112
	ds_read_b128 v[204:207], v150 offset:42560
	s_waitcnt lgkmcnt(9)
	v_mfma_f32_16x16x32_bf16 v[98:101], v[212:215], v[208:211], v[98:101]
	v_mfma_f32_16x16x32_bf16 v[94:97], v[216:219], v[208:211], v[94:97]
	ds_read_b128 v[208:211], v149 offset:384
	ds_read_b128 v[212:215], v150 offset:34176
	ds_read_b128 v[216:219], v150 offset:42624
	s_waitcnt lgkmcnt(9)
	v_mfma_f32_16x16x32_bf16 v[98:101], v[228:231], v[224:227], v[98:101]
	v_mfma_f32_16x16x32_bf16 v[94:97], v[232:235], v[224:227], v[94:97]
	ds_read_b128 v[224:227], v149 offset:448
	ds_read_b128 v[228:231], v150 offset:34240
	ds_read_b128 v[232:235], v150 offset:42688
	s_waitcnt lgkmcnt(9)
	v_mfma_f32_16x16x32_bf16 v[98:101], v[184:187], v[102:105], v[98:101]
	v_mfma_f32_16x16x32_bf16 v[94:97], v[188:191], v[102:105], v[94:97]
	s_waitcnt lgkmcnt(6)
	v_mfma_f32_16x16x32_bf16 v[98:101], v[200:203], v[192:195], v[98:101]
	v_mfma_f32_16x16x32_bf16 v[94:97], v[204:207], v[192:195], v[94:97]
	s_waitcnt lgkmcnt(3)
	v_mfma_f32_16x16x32_bf16 v[98:101], v[212:215], v[208:211], v[98:101]
	v_mfma_f32_16x16x32_bf16 v[94:97], v[216:219], v[208:211], v[94:97]
	s_waitcnt lgkmcnt(0)
	v_mfma_f32_16x16x32_bf16 v[98:101], v[228:231], v[224:227], v[98:101]
	v_mfma_f32_16x16x32_bf16 v[94:97], v[232:235], v[224:227], v[94:97]
.Lqk_done:
.LBB0_447:
	v_lshl_add_u32 v184, v132, 2, s60
	s_waitcnt lgkmcnt(0)
	ds_read_b128 v[102:105], v184
	v_readlane_b32 s28, v255, 38
	v_readlane_b32 s29, v255, 39
	s_waitcnt lgkmcnt(0)
	v_sub_f32_e32 v102, v102, v183
	v_mul_f32_e32 v102, 0x3fb8aa3b, v102
	v_exp_f32_e32 v102, v102
	v_sub_f32_e32 v103, v103, v183
	v_sub_f32_e32 v104, v104, v183
	v_mul_f32_e32 v103, 0x3fb8aa3b, v103
	v_mul_f32_e32 v98, v98, v102
	v_sub_f32_e32 v102, v105, v183
	v_exp_f32_e32 v103, v103
	v_mul_f32_e32 v104, 0x3fb8aa3b, v104
	v_mul_f32_e32 v102, 0x3fb8aa3b, v102
	v_exp_f32_e32 v104, v104
	v_exp_f32_e32 v102, v102
	v_mul_f32_e32 v99, v99, v103
	v_cndmask_b32_e64 v98, v98, 0, s[28:29]
	v_cndmask_b32_e64 v99, 0, v99, s[14:15]
	v_mul_f32_e32 v100, v100, v104
	v_mul_f32_e32 v101, v101, v102
	v_cndmask_b32_e64 v100, v100, 0, s[16:17]
	v_cndmask_b32_e64 v101, v101, 0, s[18:19]
	v_cvt_pk_bf16_f32 v98, v98, v99
	v_cvt_pk_bf16_f32 v99, v100, v101
	ds_write_b64 v144, v[98:99]
	ds_read_b128 v[98:101], v184 offset:64
	s_mul_i32 s28, s6, 0x4620
	s_add_i32 s28, s28, 0
	s_add_i32 s28, s28, 0x10800
	s_waitcnt lgkmcnt(0)
	v_sub_f32_e32 v98, v98, v183
	v_sub_f32_e32 v99, v99, v183
	v_mul_f32_e32 v98, 0x3fb8aa3b, v98
	v_mul_f32_e32 v99, 0x3fb8aa3b, v99
	v_exp_f32_e32 v98, v98
	v_exp_f32_e32 v99, v99
	v_mul_f32_e32 v94, v94, v98
	v_mul_f32_e32 v95, v95, v99
	v_sub_f32_e32 v98, v100, v183
	v_sub_f32_e32 v99, v101, v183
	v_mul_f32_e32 v98, 0x3fb8aa3b, v98
	v_mul_f32_e32 v99, 0x3fb8aa3b, v99
	v_exp_f32_e32 v98, v98
	v_exp_f32_e32 v99, v99
	v_cndmask_b32_e64 v94, v94, 0, s[20:21]
	v_cndmask_b32_e64 v95, v95, 0, s[22:23]
	v_mul_f32_e32 v96, v96, v98
	v_mul_f32_e32 v97, v97, v99
	v_cndmask_b32_e64 v96, v96, 0, s[24:25]
	v_cndmask_b32_e64 v97, v97, 0, s[26:27]
	v_cvt_pk_bf16_f32 v94, v94, v95
	v_cvt_pk_bf16_f32 v95, v96, v97
	ds_write_b64 v145, v[94:95]
	s_waitcnt lgkmcnt(0)
	s_barrier
	v_add3_u32 v183, s28, v135, v131
	ds_read_b128 v[94:97], v183 offset:16896
	ds_read_b128 v[98:101], v149
	ds_read_b128 v[102:105], v183 offset:16960
	ds_read_b128 v[184:187], v149 offset:64
	s_waitcnt lgkmcnt(2)
	v_mfma_f32_16x16x32_bf16 v[94:97], v[94:97], v[98:101], 0
	ds_read_b128 v[188:191], v183 offset:17024
	ds_read_b128 v[192:195], v149 offset:128
	s_waitcnt lgkmcnt(2)
	v_mfma_f32_16x16x32_bf16 v[94:97], v[102:105], v[184:187], v[94:97]
	ds_read_b128 v[102:105], v183 offset:17088
	ds_read_b128 v[200:203], v149 offset:192
	s_waitcnt lgkmcnt(2)
	v_mfma_f32_16x16x32_bf16 v[94:97], v[188:191], v[192:195], v[94:97]
	ds_read_b128 v[188:191], v183 offset:17152
	ds_read_b128 v[204:207], v149 offset:256
	s_waitcnt lgkmcnt(2)
	v_mfma_f32_16x16x32_bf16 v[94:97], v[102:105], v[200:203], v[94:97]
	ds_read_b128 v[102:105], v183 offset:17216
	ds_read_b128 v[208:211], v149 offset:320
	s_waitcnt lgkmcnt(2)
	v_mfma_f32_16x16x32_bf16 v[94:97], v[188:191], v[204:207], v[94:97]
	ds_read_b128 v[188:191], v183 offset:17280
	ds_read_b128 v[212:215], v149 offset:384
	s_waitcnt lgkmcnt(2)
	v_mfma_f32_16x16x32_bf16 v[94:97], v[102:105], v[208:211], v[94:97]
	ds_read_b128 v[102:105], v183 offset:17344
	ds_read_b128 v[216:219], v149 offset:448
	v_add_u32_e32 v183, v133, v131
	s_waitcnt lgkmcnt(2)
	v_mfma_f32_16x16x32_bf16 v[94:97], v[188:191], v[212:215], v[94:97]
	v_add_u32_e32 v188, v138, v136
	ds_read_b64_tr_b16 v[190:191], v188 offset:320
	ds_read_b64_tr_b16 v[188:189], v188
	ds_read_b128 v[224:227], v183
	s_waitcnt lgkmcnt(3)
	v_mfma_f32_16x16x32_bf16 v[94:97], v[102:105], v[216:219], v[94:97]
	s_waitcnt lgkmcnt(0)
	v_mfma_f32_16x16x32_bf16 v[188:191], v[188:191], v[224:227], 0
	s_nop 5
	v_add_u32_e32 v95, v138, v137
	ds_read_b64_tr_b16 v[102:103], v95 offset:64
	ds_read_b64_tr_b16 v[104:105], v95 offset:384
	v_add_u32_e32 v95, v139, v136
	ds_read_b64_tr_b16 v[230:231], v95 offset:320
	ds_read_b64_tr_b16 v[228:229], v95
	ds_read_b128 v[232:235], v146
	v_add_u32_e32 v95, v139, v137
	s_waitcnt lgkmcnt(3)
	v_mfma_f32_16x16x32_bf16 v[102:105], v[102:105], v[224:227], 0
	ds_read_b64_tr_b16 v[224:225], v95 offset:64
	ds_read_b64_tr_b16 v[226:227], v95 offset:384
	v_add3_u32 v95, s28, v134, v131
	s_waitcnt lgkmcnt(2)
	v_mfma_f32_16x16x32_bf16 v[188:191], v[228:231], v[232:235], v[188:191]
	ds_read_b128 v[228:231], v95
	s_waitcnt lgkmcnt(1)
	v_mfma_f32_16x16x32_bf16 v[102:105], v[224:227], v[232:235], v[102:105]
	ds_read_b128 v[224:227], v95 offset:64
	s_waitcnt lgkmcnt(1)
	v_mfma_f32_16x16x32_bf16 v[96:99], v[228:231], v[98:101], 0
	ds_read_b128 v[228:231], v95 offset:128
	s_waitcnt lgkmcnt(1)
	v_mfma_f32_16x16x32_bf16 v[96:99], v[224:227], v[184:187], v[96:99]
	ds_read_b128 v[184:187], v95 offset:192
	s_waitcnt lgkmcnt(1)
	v_mfma_f32_16x16x32_bf16 v[96:99], v[228:231], v[192:195], v[96:99]
	ds_read_b128 v[192:195], v95 offset:256
	s_waitcnt lgkmcnt(1)
	v_mfma_f32_16x16x32_bf16 v[96:99], v[184:187], v[200:203], v[96:99]
	ds_read_b128 v[184:187], v95 offset:320
	s_waitcnt lgkmcnt(1)
	v_mfma_f32_16x16x32_bf16 v[96:99], v[192:195], v[204:207], v[96:99]
	ds_read2st64_b32 v[104:105], v182 offset0:2 offset1:3
	ds_read_b128 v[192:195], v95 offset:384
	s_waitcnt lgkmcnt(1)
	v_fmac_f32_e32 v102, v94, v104
	ds_bpermute_b32 v182, v151, v102
	v_mfma_f32_16x16x32_bf16 v[96:99], v[184:187], v[208:211], v[96:99]
	ds_read_b128 v[100:103], v95 offset:448
	s_waitcnt lgkmcnt(2)
	v_mfma_f32_16x16x32_bf16 v[94:97], v[192:195], v[212:215], v[96:99]
	s_waitcnt lgkmcnt(0)
	v_mfma_f32_16x16x32_bf16 v[94:97], v[100:103], v[216:219], v[94:97]
	s_nop 2
	v_max_f32_e64 v98, |v182|, |v182|
	v_max_f32_e32 v99, v105, v105
	v_max_f32_e32 v98, v98, v99
	v_div_scale_f32 v99, s[28:29], v98, v98, 1.0
	v_rcp_f32_e32 v105, v99
	v_fma_f32 v94, v94, v104, v188
	v_fma_f32 v95, v95, v104, v189
	v_fma_f32 v96, v96, v104, v190
	v_fma_f32 v100, -v99, v105, 1.0
	v_fmac_f32_e32 v105, v100, v105
	v_div_scale_f32 v100, vcc, 1.0, v98, 1.0
	v_mul_f32_e32 v101, v100, v105
	v_fma_f32 v102, -v99, v101, v100
	v_fmac_f32_e32 v101, v102, v105
	v_fma_f32 v99, -v99, v101, v100
	v_div_fmas_f32 v99, v99, v105, v101
	v_div_fixup_f32 v98, v99, v98, 1.0
	v_fmac_f32_e32 v191, v97, v104
	v_mov_b32_e32 v182, s60
	v_mul_f32_e32 v94, v94, v98
	v_mul_f32_e32 v95, v95, v98
	v_mul_f32_e32 v96, v96, v98
	v_mul_f32_e32 v97, v191, v98
	v_cvt_pk_bf16_f32 v200, v94, v95
	v_cvt_pk_bf16_f32 v201, v96, v97
	ds_read_b32 v196, v182 offset:1280
	ds_read_b64_tr_b16 v[94:95], v147
	ds_read_b64_tr_b16 v[98:99], v147 offset:32
	ds_read_b64_tr_b16 v[102:103], v147 offset:64
	ds_read_b64_tr_b16 v[184:185], v148 offset:35904
	ds_read_b64_tr_b16 v[182:183], v148 offset:33792
	ds_read_b64_tr_b16 v[96:97], v147 offset:320
	ds_read_b64_tr_b16 v[100:101], v147 offset:352
	ds_read_b64_tr_b16 v[104:105], v147 offset:384
	ds_read_b64_tr_b16 v[186:187], v147 offset:2560
	ds_read_b64_tr_b16 v[188:189], v148 offset:33824
	ds_read_b64_tr_b16 v[192:193], v147 offset:2944
	ds_read_b64_tr_b16 v[190:191], v148 offset:35936
	s_waitcnt lgkmcnt(12)
	v_pk_mul_f32 v[88:89], v[88:89], v[196:197] op_sel_hi:[1,0]
	v_pk_mul_f32 v[86:87], v[86:87], v[196:197] op_sel_hi:[1,0]
	v_pk_mul_f32 v[84:85], v[84:85], v[196:197] op_sel_hi:[1,0]
	v_pk_mul_f32 v[82:83], v[82:83], v[196:197] op_sel_hi:[1,0]
	v_pk_mul_f32 v[76:77], v[76:77], v[196:197] op_sel_hi:[1,0]
	v_pk_mul_f32 v[74:75], v[74:75], v[196:197] op_sel_hi:[1,0]
	v_pk_mul_f32 v[80:81], v[80:81], v[196:197] op_sel_hi:[1,0]
	v_pk_mul_f32 v[78:79], v[78:79], v[196:197] op_sel_hi:[1,0]
	v_pk_mul_f32 v[72:73], v[72:73], v[196:197] op_sel_hi:[1,0]
	v_pk_mul_f32 v[70:71], v[70:71], v[196:197] op_sel_hi:[1,0]
	v_pk_mul_f32 v[68:69], v[68:69], v[196:197] op_sel_hi:[1,0]
	v_pk_mul_f32 v[66:67], v[66:67], v[196:197] op_sel_hi:[1,0]
	s_waitcnt lgkmcnt(6)
	v_mfma_f32_16x16x32_bf16 v[86:89], v[182:185], v[94:97], v[86:89]
	s_add_i32 s28, s47, 0xffffff00
	s_cmp_lt_u32 s7, 4
	s_cselect_b32 s7, s47, s28
	s_waitcnt lgkmcnt(5)
	v_mfma_f32_16x16x32_bf16 v[82:85], v[182:185], v[98:101], v[82:85]
	s_waitcnt lgkmcnt(4)
	v_mfma_f32_16x16x32_bf16 v[74:77], v[182:185], v[102:105], v[74:77]
	ds_read_b64_tr_b16 v[182:183], v148 offset:50688
	ds_read_b64_tr_b16 v[194:195], v148 offset:50720
	ds_read_b64_tr_b16 v[184:185], v148 offset:52800
	s_waitcnt lgkmcnt(3)
	v_mfma_f32_16x16x32_bf16 v[78:81], v[188:191], v[94:97], v[78:81]
	v_mfma_f32_16x16x32_bf16 v[70:73], v[188:191], v[98:101], v[70:73]
	v_add_u32_e32 v98, s7, v130
	s_movk_i32 s7, 0xfff
	s_cselect_b32 s7, 0xff, s7
	v_mfma_f32_16x16x32_bf16 v[66:69], v[188:191], v[102:105], v[66:69]
	ds_read_b64_tr_b16 v[188:189], v147 offset:2880
	ds_read_b64_tr_b16 v[96:97], v147 offset:2912
	ds_read_b64_tr_b16 v[190:191], v147 offset:2624
	ds_read_b64_tr_b16 v[94:95], v147 offset:2592
	ds_read_b64_tr_b16 v[196:197], v148 offset:52832
	v_sub_u32_e32 v99, s7, v98
	v_cndmask_b32_e64 v98, v99, v98, s[2:3]
	s_cselect_b32 s7, s45, s48
	v_add_u32_e32 v98, s7, v98
	v_ashrrev_i32_e32 v99, 31, v98
	s_waitcnt lgkmcnt(4)
	v_mfma_f32_16x16x32_bf16 v[86:89], v[182:185], v[186:189], v[86:89]
	s_xor_b32 s6, s6, 1
	s_mul_i32 s7, s6, 0x4620
	s_waitcnt lgkmcnt(1)
	v_mfma_f32_16x16x32_bf16 v[82:85], v[182:185], v[94:97], v[82:85]
	v_mfma_f32_16x16x32_bf16 v[74:77], v[182:185], v[190:193], v[74:77]
	s_waitcnt lgkmcnt(0)
	v_mfma_f32_16x16x32_bf16 v[78:81], v[194:197], v[186:189], v[78:81]
	v_mfma_f32_16x16x32_bf16 v[70:73], v[194:197], v[94:97], v[70:73]
	v_lshlrev_b64 v[94:95], 11, v[98:99]
	v_lshl_add_u64 v[94:95], v[110:111], 0, v[94:95]
	global_store_dwordx2 v[94:95], v[200:201], off
	v_mfma_f32_16x16x32_bf16 v[66:69], v[194:197], v[190:193], v[66:69]
	v_add_u32_e32 v94, s7, v140
	v_cvt_pk_bf16_f32 v96, v86, v87
	v_cvt_pk_bf16_f32 v97, v88, v89
	v_add_u32_e32 v95, v94, v135
	ds_write_b64 v95, v[96:97]
	v_cvt_pk_bf16_f32 v96, v82, v83
	v_cvt_pk_bf16_f32 v97, v84, v85
	ds_write_b64 v95, v[96:97] offset:8448
	s_and_saveexec_b64 s[28:29], s[8:9]
	s_cbranch_execz .LBB0_449
	v_cvt_pk_bf16_f32 v96, v74, v75
	v_cvt_pk_bf16_f32 v97, v76, v77
	ds_write_b64 v94, v[96:97] offset:16896

.LBB0_455:
	s_lshl_b32 s7, s92, 22
	s_lshl_b32 s7, s7, 1
	s_add_u32 s7, s35, s7
	s_addc_u32 s28, s33, 0
	s_add_u32 s29, s56, s12
	s_addc_u32 s30, s39, 0
	s_cmp_eq_u32 s11, 2
	s_cselect_b32 s7, s7, s29
	s_cselect_b32 s30, s28, s30
	s_and_b64 s[28:29], s[90:91], exec
	s_mov_b32 s12, 0x2400000
	v_readlane_b32 s80, v254, 36
	s_cselect_b32 s28, s12, 0x4300000
	v_readlane_b32 s86, v254, 42
	v_readlane_b32 s87, v254, 43
	s_add_u32 s31, s86, s28
	s_addc_u32 s60, s87, 0
	s_and_b64 s[28:29], s[52:53], exec
	s_cselect_b32 s29, s60, s30
	s_cselect_b32 s28, s31, s7
	s_lshl_b32 s7, s43, 1
	s_and_b32 s30, s46, 0x60
	s_lshl_b32 s31, s11, 7
	s_and_b32 s7, s7, 0xf00
	s_or_b32 s30, s31, s30
	s_add_i32 s30, s30, s7
	s_cmp_gt_i32 s11, 1
	s_cselect_b32 s7, s43, s30
	s_ashr_i32 s11, s7, 3
	s_andn2_b32 s11, s11, 31
	s_or_b32 s30, s11, s50
	s_ashr_i32 s31, s30, 31
	s_lshl_b64 s[30:31], s[30:31], 8
	s_and_b32 s7, s7, 0xe0
	s_or_b32 s7, s30, s7
	s_mov_b32 s100, s7
	s_mov_b32 s101, s31
	s_lshl_b64 s[100:101], s[100:101], 7
	s_add_u32 s100, s100, s28
	s_addc_u32 s101, s101, s29
	s_waitcnt vmcnt(1)
	v_cvt_pk_bf16_f32 v152, v152, v156
	v_cvt_pk_bf16_f32 v156, v153, v157
	v_cvt_pk_bf16_f32 v238, v154, v158
	v_cvt_pk_bf16_f32 v242, v155, v159
	v_cvt_pk_bf16_f32 v153, v160, v164
	v_cvt_pk_bf16_f32 v157, v161, v165
	v_cvt_pk_bf16_f32 v239, v162, v166
	v_cvt_pk_bf16_f32 v243, v163, v167
	v_cvt_pk_bf16_f32 v154, v168, v172
	v_cvt_pk_bf16_f32 v158, v169, v173
	v_cvt_pk_bf16_f32 v240, v170, v174
	v_cvt_pk_bf16_f32 v244, v171, v175
	v_cvt_pk_bf16_f32 v155, v176, v246
	v_cvt_pk_bf16_f32 v159, v177, v247
	v_cvt_pk_bf16_f32 v241, v178, v248
	v_cvt_pk_bf16_f32 v245, v179, v249
	global_store_dwordx4 v251, v[152:155], s[100:101]
	global_store_dwordx4 v251, v[156:159], s[100:101] offset:128
	global_store_dwordx4 v251, v[238:241], s[100:101] offset:256
	global_store_dwordx4 v251, v[242:245], s[100:101] offset:384
	s_andn2_b64 vcc, exec, s[94:95]
	s_mov_b32 s86, s38
	v_readlane_b32 s81, v254, 37
	v_readlane_b32 s82, v254, 38
	v_readlane_b32 s83, v254, 39
	v_readlane_b32 s84, v254, 40
	v_readlane_b32 s85, v254, 41
	s_cbranch_vccnz .LBB0_410
	s_lshl_b32 s7, s13, 1
	s_add_u32 s7, s35, s7
	s_addc_u32 s11, s33, 0
	s_lshl_b32 s28, s93, 24
	s_add_u32 s28, s56, s28
	s_addc_u32 s29, s39, 0
	s_cmp_eq_u32 s57, 2
	s_cselect_b32 s7, s7, s28
	s_cselect_b32 s11, s11, s29
	s_and_b64 s[0:1], s[0:1], exec
	s_mov_b32 s0, 0x2400000
	v_readlane_b32 s72, v254, 36
	s_cselect_b32 s0, s0, 0x4300000
	v_readlane_b32 s78, v254, 42
	v_readlane_b32 s79, v254, 43
	s_add_u32 s28, s78, s0
	s_addc_u32 s29, s79, 0
	s_and_b64 s[0:1], s[96:97], exec
	s_cselect_b32 s1, s29, s11
	s_cselect_b32 s0, s28, s7
	s_lshl_b32 s7, s37, 1
	s_and_b32 s11, s34, 0x60
	s_lshl_b32 s28, s57, 7
	s_and_b32 s7, s7, 0xf00
	s_or_b32 s11, s28, s11
	s_add_i32 s11, s11, s7
	s_cmp_gt_i32 s57, 1
	s_cselect_b32 s7, s37, s11
	s_ashr_i32 s11, s7, 3
	s_andn2_b32 s11, s11, 31
	s_lshr_b32 s28, s36, 6
	s_or_b32 s28, s11, s28
	s_ashr_i32 s29, s28, 31
	s_lshl_b64 s[28:29], s[28:29], 8
	s_and_b32 s7, s7, 0xe0
	s_or_b32 s7, s28, s7
	v_readlane_b32 s73, v254, 37
	v_readlane_b32 s74, v254, 38
	v_readlane_b32 s75, v254, 39
	v_readlane_b32 s76, v254, 40
	v_readlane_b32 s77, v254, 41
	s_mov_b32 s100, s7
	s_mov_b32 s101, s29
	s_lshl_b64 s[100:101], s[100:101], 7
	s_add_u32 s100, s100, s0
	s_addc_u32 s101, s101, s1
	v_cvt_pk_bf16_f32 v2, v2, v6
	v_cvt_pk_bf16_f32 v6, v3, v7
	v_cvt_pk_bf16_f32 v238, v4, v8
	v_cvt_pk_bf16_f32 v242, v5, v9
	v_cvt_pk_bf16_f32 v3, v10, v14
	v_cvt_pk_bf16_f32 v7, v11, v15
	v_cvt_pk_bf16_f32 v239, v12, v16
	v_cvt_pk_bf16_f32 v243, v13, v17
	v_cvt_pk_bf16_f32 v4, v18, v22
	v_cvt_pk_bf16_f32 v8, v19, v23
	v_cvt_pk_bf16_f32 v240, v20, v24
	v_cvt_pk_bf16_f32 v244, v21, v25
	v_cvt_pk_bf16_f32 v5, v26, v116
	v_cvt_pk_bf16_f32 v9, v27, v117
	v_cvt_pk_bf16_f32 v241, v28, v118
	v_cvt_pk_bf16_f32 v245, v29, v119
	global_store_dwordx4 v251, v[2:5], s[100:101]
	global_store_dwordx4 v251, v[6:9], s[100:101] offset:128
	global_store_dwordx4 v251, v[238:241], s[100:101] offset:256
	global_store_dwordx4 v251, v[242:245], s[100:101] offset:384
	s_branch .LBB0_410
.LBB0_469:
	v_readlane_b32 s85, v255, 6
	v_mov_b32_e32 v2, v0
	s_cmpk_gt_i32 s85, 0x10f
	v_readlane_b32 s84, v255, 5
	v_readfirstlane_b32 s0, v2
	v_readlane_b32 s87, v255, 4
	s_cbranch_scc1 .LBB0_485
	v_ashrrev_i32_e32 v3, 31, v2
	v_lshrrev_b32_e32 v3, 26, v3
	v_add_u32_e32 v3, v2, v3
	v_ashrrev_i32_e32 v5, 6, v3
	v_bfe_i32 v3, v2, 27, 1
	v_lshlrev_b32_e32 v1, 4, v2
	v_lshrrev_b32_e32 v3, 22, v3
	v_add_u32_e32 v3, v1, v3
	v_and_b32_e32 v3, 0xfffffc00, v3
	v_sub_u32_e32 v3, v1, v3
	v_lshrrev_b32_e32 v4, 4, v3
	v_bitop3_b32 v3, v4, v3, 32 bitop3:0x6c
	v_ashrrev_i32_e32 v6, 31, v3
	v_lshrrev_b32_e32 v6, 26, v6
	v_add_u32_e32 v6, v3, v6
	v_ashrrev_i32_e32 v7, 6, v6
	v_and_b32_e32 v6, 0xc0, v6
	v_sub_u32_e32 v3, v3, v6
	v_mov_b32_e32 v6, 1
	v_lshlrev_b32_e32 v4, 5, v5
	v_ashrrev_i16_sdwa v3, v6, sext(v3) dst_sel:DWORD dst_unused:UNUSED_PAD src0_sel:DWORD src1_sel:BYTE_0
	v_and_b32_e32 v4, 32, v4
	v_bfe_i32 v3, v3, 0, 16
	v_add_u32_e32 v1, 0x2000, v1
	v_add_lshl_u32 v3, v4, v3, 1
	v_ashrrev_i32_e32 v4, 31, v1
	v_lshrrev_b32_e32 v4, 22, v4
	v_add_u32_e32 v4, v1, v4
	v_ashrrev_i32_e32 v8, 10, v4
	v_mul_i32_i24_e32 v4, 0x400, v8
	v_sub_u32_e32 v1, v1, v4
	v_lshrrev_b32_e32 v4, 4, v1
	v_bitop3_b32 v1, v4, v1, 32 bitop3:0x6c
	v_ashrrev_i32_e32 v9, 31, v1
	v_lshrrev_b32_e32 v9, 26, v9
	v_readlane_b32 s4, v254, 36
	v_add_u32_e32 v9, v1, v9
	v_readlane_b32 s5, v254, 37
	v_readlane_b32 s6, v254, 38
	v_readlane_b32 s7, v254, 39
	v_readlane_b32 s8, v254, 40
	v_readlane_b32 s9, v254, 41
	v_ashrrev_i32_e32 v10, 6, v9
	v_and_b32_e32 v9, 0xc0, v9
	s_ashr_i32 s2, s0, 6
	v_readlane_b32 s10, v254, 42
	v_readlane_b32 s11, v254, 43
	s_mov_b64 s[4:5], s[8:9]
	s_ashr_i32 s1, s0, 8
	v_sub_u32_e32 v1, v1, v9
	s_lshl_b32 s33, s2, 10
	s_mov_b64 s[6:7], s[10:11]
	v_lshlrev_b32_e32 v4, 5, v8
	v_ashrrev_i16_sdwa v1, v6, sext(v1) dst_sel:DWORD dst_unused:UNUSED_PAD src0_sel:DWORD src1_sel:BYTE_0
	s_add_u32 s4, s6, 0x58e00000
	v_and_b32_e32 v4, 32, v4
	v_bfe_i32 v1, v1, 0, 16
	s_addc_u32 s5, s7, 0
	v_add_lshl_u32 v4, v4, v1, 1
	s_add_u32 s34, s6, 0x2c00000
	v_lshlrev_b32_e32 v1, 3, v8
	s_addc_u32 s35, s7, 0
	s_and_b32 s57, s85, 3
	s_ashr_i32 s56, s85, 2
	v_and_b32_e32 v1, -16, v1
	s_lshl_b32 s3, s56, 19
	s_lshl_b32 s6, s57, 9
	v_add_u32_e32 v1, v10, v1
	s_or_b32 s3, s6, s3
	v_and_b32_e32 v6, 3, v10
	s_mov_b32 s9, 0x1ffffe0
	v_lshrrev_b32_e32 v8, 2, v1
	v_lshlrev_b32_e32 v9, 1, v1
	v_lshlrev_b32_e32 v5, 3, v5
	s_or_b32 s8, s3, 0x40000
	s_lshl_b32 s6, s57, 17
	v_and_or_b32 v6, v1, s9, v6
	v_and_b32_e32 v8, 4, v8
	v_and_b32_e32 v9, 24, v9
	v_and_b32_e32 v5, -16, v5
	s_add_u32 s22, s34, s6
	v_or3_b32 v6, v6, v8, v9
	v_add_u32_e32 v5, v7, v5
	s_addc_u32 s23, s35, 0
	v_lshl_add_u32 v146, v6, 7, v4
	v_and_b32_e32 v6, 3, v7
	v_lshrrev_b32_e32 v7, 2, v5
	v_lshlrev_b32_e32 v8, 1, v5
	s_add_u32 s6, s22, 0x4000
	v_and_or_b32 v6, v5, s9, v6
	v_and_b32_e32 v7, 4, v7
	v_and_b32_e32 v8, 24, v8
	s_addc_u32 s7, s23, 0
	v_or3_b32 v6, v6, v7, v8
	s_add_i32 s44, s33, 0
	v_lshl_add_u32 v148, v6, 7, v3
	s_add_i32 m0, s44, 0x10000
	v_lshlrev_b32_e32 v5, 11, v5
	global_load_lds_dwordx4 v148, s[22:23]
	s_add_i32 m0, s44, 0x12000
	v_add3_u32 v150, v5, s3, v3
	global_load_lds_dwordx4 v146, s[22:23]
	s_add_i32 m0, s44, 0x14000
	v_lshlrev_b32_e32 v6, 11, v1
	global_load_lds_dwordx4 v148, s[6:7]
	s_add_i32 m0, s44, 0x16000
	s_add_i32 s45, s44, 0x2000
	global_load_lds_dwordx4 v146, s[6:7]
	s_mov_b32 m0, s44
	v_add3_u32 v134, v6, s3, v4
	global_load_lds_dwordx4 v150, s[4:5]
	s_mov_b32 m0, s45
	s_add_i32 s46, s44, 0x4000
	v_add3_u32 v132, v5, s8, v3
	global_load_lds_dwordx4 v134, s[4:5]
	s_mov_b32 m0, s46
	s_add_i32 s47, s44, 0x6000
	v_add3_u32 v130, v6, s8, v4
	global_load_lds_dwordx4 v132, s[4:5]
	s_mov_b32 m0, s47
	v_mov_b32_e32 v151, 0
	global_load_lds_dwordx4 v130, s[4:5]
	s_cmp_eq_u32 s1, 1
	s_mov_b32 s48, 0
	v_mov_b32_e32 v149, v151
	v_mov_b32_e32 v147, v151
	s_cselect_b64 s[6:7], -1, 0
	s_cmp_lg_u32 s1, 1
	v_mov_b32_e32 v135, v151
	s_cbranch_scc1 .LBB0_472
	s_barrier

.LBB0_1410:
	s_ashr_i32 s2, s71, 8
	s_lshl_b32 s1, s71, 8
	s_lshl_b32 s0, s2, 12
	s_and_b32 s1, s1, 0xf00
	s_bfe_u32 s72, s71, 0x40004
	s_or_b32 s34, s0, s1
	s_lshl_b32 s66, s72, 9
	s_ashr_i32 s35, s34, 31
	s_mul_i32 s1, s34, 0x1800
	s_mul_hi_i32 s0, s34, 0x1800
	s_add_u32 s1, s25, s1
	s_addc_u32 s3, s38, s0
	s_mul_i32 s0, s72, 0x180
	s_waitcnt vmcnt(0)
	v_mov_b32_e32 v12, v0
	s_add_u32 s0, s1, s0
	s_addc_u32 s1, s3, 0
	v_ashrrev_i32_e32 v13, 6, v12
	v_and_b32_e32 v155, 31, v12
	v_lshlrev_b32_e32 v158, 5, v13
	s_waitcnt lgkmcnt(0)
	v_bfe_u32 v176, v12, 5, 1
	v_or_b32_e32 v4, v158, v155
	v_mov_b64_e32 v[2:3], s[0:1]
	v_mad_i64_i32 v[2:3], s[0:1], v4, s45, v[2:3]
	v_lshlrev_b32_e32 v156, 4, v176
	v_lshl_add_u64 v[10:11], v[2:3], 0, v[156:157]
	global_load_dwordx4 v[2:5], v[10:11], off offset:320
	global_load_dwordx4 v[6:9], v[10:11], off offset:352
	global_load_dwordx4 v[134:137], v[10:11], off
	global_load_dwordx4 v[130:133], v[10:11], off offset:32
	global_load_dwordx4 v[126:129], v[10:11], off offset:64
	global_load_dwordx4 v[122:125], v[10:11], off offset:96
	global_load_dwordx4 v[118:121], v[10:11], off offset:128
	global_load_dwordx4 v[114:117], v[10:11], off offset:160
	global_load_dwordx4 v[110:113], v[10:11], off offset:192
	global_load_dwordx4 v[106:109], v[10:11], off offset:224
	global_load_dwordx4 v[102:105], v[10:11], off offset:256
	global_load_dwordx4 v[98:101], v[10:11], off offset:288
	s_mulk_i32 s2, 0x1100
	s_ashr_i32 s3, s2, 31
	s_lshl_b64 s[0:1], s[2:3], 13
	s_add_u32 s4, s39, s0
	s_addc_u32 s5, s40, s1
	s_add_u32 s36, s4, s66
	s_addc_u32 s37, s5, 0
	s_lshl_b64 s[4:5], s[2:3], 7
	v_lshlrev_b32_e32 v59, 3, v12
	v_readfirstlane_b32 s67, v13
	s_add_u32 s2, s41, s4
	v_and_b32_e32 v52, 63, v12
	v_mul_lo_u32 v16, v13, s45
	v_and_b32_e32 v13, 24, v59
	s_addc_u32 s3, s42, s5
	s_lshl_b32 s33, s67, 3
	s_lshl_b32 s64, s67, 2
	v_lshlrev_b32_e32 v64, 4, v52
	v_add_u32_e32 v16, s47, v16
	v_and_or_b32 v56, v12, 32, v13
	v_lshl_or_b32 v13, s67, 6, v52
	s_and_b32 s73, s33, -16
	s_and_b32 s74, s64, 4
	v_bfe_u32 v15, v12, 4, 2
	v_lshrrev_b32_e32 v14, 1, v12
	v_add_u32_e32 v180, v16, v64
	v_lshlrev_b32_e32 v16, 3, v13
	v_lshrrev_b32_e32 v13, 4, v13
	s_cmp_lg_u32 0, -1
	v_and_b32_e32 v54, 8, v14
	v_lshlrev_b32_e32 v14, 12, v15
	v_xor_b32_e32 v13, v13, v12
	v_or3_b32 v11, v15, s33, 4
	s_cselect_b32 s75, 0, 0
	s_lshl_b32 s33, s67, 11
	v_and_b32_e32 v17, 15, v12
	v_bitop3_b32 v18, v15, v12, 15 bitop3:0x78
	v_lshrrev_b32_e32 v19, 3, v12
	v_and_b32_e32 v19, 8, v19
	v_xor_b32_e32 v18, v18, v19
	v_lshl_or_b32 v55, s67, 15, v14
	v_lshlrev_b32_e32 v13, 3, v13
	s_cmp_lg_u32 s49, -1
	v_bfe_u32 v53, v12, 2, 2
	v_lshl_or_b32 v14, v18, 3, v55
	v_and_b32_e32 v57, 56, v13
	v_bitop3_b32 v13, v11, v17, 15 bitop3:0x6c
	s_cselect_b32 s64, s49, 0
	v_mov_b32_e32 v15, v157
	v_or3_b32 v10, v54, v53, s73
	v_lshlrev_b32_e32 v58, 3, v13
	s_add_i32 s76, s33, s64
	s_add_i32 s64, s33, s75
	s_lshl_b32 s65, s67, 10
	v_lshlrev_b64 v[50:51], 1, v[14:15]
	v_or_b32_e32 v10, s74, v10
	v_lshl_or_b32 v18, v11, 12, v58
	s_cmp_lg_u32 s50, -1
	s_mov_b32 m0, s76
	v_mov_b32_e32 v19, v157
	v_lshl_or_b32 v10, v10, 12, v56
	s_cselect_b32 s77, s50, 0
	v_mov_b32_e32 v11, v157
	v_and_or_b32 v16, v16, s48, v57
	s_add_i32 s77, s65, s77
	s_waitcnt vmcnt(11)
	ds_write_b128 v180, v[2:5]
	s_waitcnt vmcnt(10)
	ds_write_b128 v180, v[6:9] offset:1024
	v_lshl_add_u64 v[2:3], s[36:37], 0, v[50:51]
	global_load_lds_dwordx4 v[2:3], off
	v_lshlrev_b64 v[2:3], 1, v[18:19]
	v_lshl_add_u64 v[4:5], s[36:37], 0, v[2:3]
	s_add_i32 m0, s76, 0x400
	v_mov_b32_e32 v17, v157
	v_lshlrev_b64 v[6:7], 1, v[10:11]
	global_load_lds_dwordx4 v[4:5], off
	v_lshl_add_u64 v[4:5], v[16:17], 1, s[2:3]
	s_mov_b32 m0, s77
	v_lshl_add_u64 v[8:9], s[36:37], 0, v[6:7]
	s_mov_b64 s[2:3], 0x100
	v_or_b32_e32 v20, 64, v10
	global_load_lds_dwordx4 v[4:5], off
	v_lshl_add_u64 v[10:11], v[8:9], 0, s[2:3]
	s_mov_b32 m0, s64
	s_mov_b64 s[2:3], 0x180
	global_load_lds_dwordx4 v[10:11], off
	s_add_i32 m0, s64, 0x400
	v_lshl_add_u64 v[8:9], v[8:9], 0, s[2:3]
	s_add_u32 s2, s36, 0x80000
	s_addc_u32 s3, s37, 0
	global_load_lds_dwordx4 v[8:9], off
	v_lshl_add_u64 v[8:9], s[2:3], 0, v[50:51]
	s_add_i32 m0, s76, 0x4000
	v_lshl_add_u64 v[2:3], s[2:3], 0, v[2:3]
	global_load_lds_dwordx4 v[8:9], off
	s_add_i32 m0, s76, 0x4400
	s_mov_b64 s[2:3], 0x2000
	global_load_lds_dwordx4 v[2:3], off
	s_add_i32 m0, s77, 0x2000
	v_lshl_add_u64 v[2:3], v[4:5], 0, s[2:3]
	s_add_u32 s2, s36, 0x80100
	s_addc_u32 s3, s37, 0
	v_mov_b32_e32 v21, v157
	global_load_lds_dwordx4 v[2:3], off
	v_lshl_add_u64 v[2:3], s[2:3], 0, v[6:7]
	s_add_i32 m0, s64, 0x4000
	v_lshlrev_b32_e32 v10, 8, v155
	global_load_lds_dwordx4 v[2:3], off
	v_lshl_add_u64 v[2:3], v[20:21], 1, s[2:3]
	s_add_i32 m0, s64, 0x4400
	v_or_b32_e32 v13, 32, v156
	global_load_lds_dwordx4 v[2:3], off
	v_lshlrev_b32_e32 v2, 4, v12
	v_and_b32_e32 v11, 0xf0, v2
	v_bitop3_b32 v182, v156, v10, v11 bitop3:0xde
	v_add_u32_e32 v183, 0, v182
	s_waitcnt vmcnt(0)
	s_waitcnt vmcnt(0) lgkmcnt(0)
	s_barrier
	ds_read_b128 v[2:5], v183 offset:49152
	ds_read_b128 v[6:9], v183 offset:57344
	s_waitcnt lgkmcnt(1)
	v_mfma_f32_32x32x16_bf16 v[34:49], v[2:5], v[134:137], 0
	v_bitop3_b32 v184, v13, v10, v11 bitop3:0xde
	v_add_u32_e32 v185, 0, v184
	v_or_b32_e32 v14, 64, v156
	v_bitop3_b32 v186, v14, v10, v11 bitop3:0xde
	v_add_u32_e32 v187, 0, v186
	v_or_b32_e32 v65, 0x60, v156
	v_bitop3_b32 v188, v65, v10, v11 bitop3:0xde
	s_waitcnt lgkmcnt(0)
	v_mfma_f32_32x32x16_bf16 v[18:33], v[6:9], v[134:137], 0
	ds_read_b128 v[2:5], v185 offset:49152
	ds_read_b128 v[6:9], v185 offset:57344
	v_add_u32_e32 v189, 0, v188
	v_cmp_gt_u32_e64 s[2:3], 32, v52
	s_mov_b32 s36, -1
	s_mov_b32 s37, 0
	v_mov_b32_e32 v178, 0
	s_waitcnt lgkmcnt(1)
	v_mfma_f32_32x32x16_bf16 v[34:49], v[2:5], v[130:133], v[34:49]
	s_waitcnt lgkmcnt(0)
	v_mfma_f32_32x32x16_bf16 v[18:33], v[6:9], v[130:133], v[18:33]
	ds_read_b128 v[2:5], v187 offset:49152
	ds_read_b128 v[6:9], v187 offset:57344
	s_waitcnt lgkmcnt(1)
	v_mfma_f32_32x32x16_bf16 v[34:49], v[2:5], v[126:129], v[34:49]
	s_waitcnt lgkmcnt(0)
	v_mfma_f32_32x32x16_bf16 v[18:33], v[6:9], v[126:129], v[18:33]
	ds_read_b128 v[2:5], v189 offset:49152
	ds_read_b128 v[6:9], v189 offset:57344
	s_waitcnt lgkmcnt(1)
	v_mfma_f32_32x32x16_bf16 v[34:49], v[2:5], v[122:125], v[34:49]
	v_or_b32_e32 v2, 0x80, v156
	v_bitop3_b32 v190, v2, v10, v11 bitop3:0xde
	v_add_u32_e32 v191, 0, v190
	s_waitcnt lgkmcnt(0)
	v_mfma_f32_32x32x16_bf16 v[18:33], v[6:9], v[122:125], v[18:33]
	ds_read_b128 v[2:5], v191 offset:49152
	ds_read_b128 v[6:9], v191 offset:57344
	s_waitcnt lgkmcnt(1)
	v_mfma_f32_32x32x16_bf16 v[34:49], v[2:5], v[118:121], v[34:49]
	v_or_b32_e32 v2, 0xa0, v156
	v_bitop3_b32 v192, v2, v10, v11 bitop3:0xde
	v_add_u32_e32 v193, 0, v192
	s_waitcnt lgkmcnt(0)
	v_mfma_f32_32x32x16_bf16 v[18:33], v[6:9], v[118:121], v[18:33]
	ds_read_b128 v[2:5], v193 offset:49152
	ds_read_b128 v[6:9], v193 offset:57344
	s_waitcnt lgkmcnt(1)
	v_mfma_f32_32x32x16_bf16 v[34:49], v[2:5], v[114:117], v[34:49]
	v_or_b32_e32 v2, 0xc0, v156
	v_bitop3_b32 v194, v2, v10, v11 bitop3:0xde
	v_add_u32_e32 v195, 0, v194
	s_waitcnt lgkmcnt(0)
	v_mfma_f32_32x32x16_bf16 v[18:33], v[6:9], v[114:117], v[18:33]
	ds_read_b128 v[2:5], v195 offset:49152
	ds_read_b128 v[6:9], v195 offset:57344
	s_waitcnt lgkmcnt(1)
	v_mfma_f32_32x32x16_bf16 v[34:49], v[2:5], v[110:113], v[34:49]
	v_or_b32_e32 v2, 0xe0, v156
	v_bitop3_b32 v196, v2, v10, v11 bitop3:0xde
	v_add_u32_e32 v197, 0, v196
	v_lshlrev_b32_e32 v10, 7, v155
	v_and_b32_e32 v11, 0x70, v59
	v_bitop3_b32 v199, v156, v10, v11 bitop3:0xde
	v_add_u32_e32 v200, s50, v199
	s_waitcnt lgkmcnt(0)
	v_mfma_f32_32x32x16_bf16 v[18:33], v[6:9], v[110:113], v[18:33]
	ds_read_b128 v[2:5], v197 offset:49152
	ds_read_b128 v[6:9], v197 offset:57344
	v_bitop3_b32 v201, v13, v10, v11 bitop3:0xde
	v_add_u32_e32 v202, s50, v201
	v_bitop3_b32 v203, v14, v10, v11 bitop3:0xde
	v_add_u32_e32 v204, s50, v203
	v_bitop3_b32 v205, v65, v10, v11 bitop3:0xde
	v_add_u32_e32 v206, s50, v205
	s_waitcnt lgkmcnt(1)
	v_mfma_f32_32x32x16_bf16 v[34:49], v[2:5], v[106:109], v[34:49]
	v_lshlrev_b32_e32 v59, 3, v52
	s_waitcnt lgkmcnt(0)
	v_mfma_f32_32x32x16_bf16 v[18:33], v[6:9], v[106:109], v[18:33]
	ds_read_b128 v[2:5], v200
	ds_read_b128 v[6:9], v200 offset:4096
	s_waitcnt lgkmcnt(1)
	v_mfma_f32_32x32x16_bf16 v[34:49], v[2:5], v[102:105], v[34:49]
	s_waitcnt lgkmcnt(0)
	v_mfma_f32_32x32x16_bf16 v[18:33], v[6:9], v[102:105], v[18:33]
	ds_read_b128 v[2:5], v202
	ds_read_b128 v[6:9], v202 offset:4096
	s_waitcnt lgkmcnt(1)
	v_mfma_f32_32x32x16_bf16 v[34:49], v[2:5], v[98:101], v[34:49]
	s_waitcnt lgkmcnt(0)
	v_mfma_f32_32x32x16_bf16 v[18:33], v[6:9], v[98:101], v[18:33]
	ds_read_b128 v[2:5], v204
	ds_read_b128 v[6:9], v180
	ds_read_b128 v[14:17], v204 offset:4096
	ds_read_b128 v[60:63], v180 offset:1024
	s_waitcnt lgkmcnt(2)
	v_mfma_f32_32x32x16_bf16 v[34:49], v[2:5], v[6:9], v[34:49]
	ds_read_b128 v[2:5], v206
	s_waitcnt lgkmcnt(2)
	v_mfma_f32_32x32x16_bf16 v[18:33], v[14:17], v[6:9], v[18:33]
	v_and_b32_e32 v6, 0x3fffffc0, v12
	v_lshl_add_u32 v159, v6, 2, s46
	v_and_b32_e32 v6, 0xc0, v64
	ds_read_b128 v[64:67], v206 offset:4096
	v_lshl_add_u32 v177, v155, 2, v159
	s_waitcnt lgkmcnt(0)
	s_barrier
	v_mfma_f32_32x32x16_bf16 v[34:49], v[2:5], v[60:63], v[34:49]
	v_lshlrev_b32_e32 v3, 1, v12
	v_and_or_b32 v2, v59, 24, v6
	v_and_b32_e32 v3, 32, v3
	v_and_b32_e32 v4, 0x100, v59
	v_or3_b32 v179, v2, v3, v4
	v_mov_b64_e32 v[2:3], s[8:9]
	v_mov_b64_e32 v[16:17], s[22:23]
	v_mfma_f32_32x32x16_bf16 v[18:33], v[64:67], v[60:63], v[18:33]
	s_nop 3
	v_max_f32_e32 v60, v35, v35
	v_max_f32_e32 v61, v34, v34
	v_max_f32_e32 v60, v61, v60
	v_max3_f32 v60, v60, v36, v37
	v_max3_f32 v60, v60, v38, v39
	v_max3_f32 v60, v60, v40, v41
	v_max3_f32 v60, v60, v42, v43
	v_max3_f32 v60, v60, v44, v45
	v_max3_f32 v60, v60, v46, v47
	v_max3_f32 v60, v60, v48, v49
	v_max3_f32 v60, v60, v18, v19
	v_max3_f32 v60, v60, v20, v21
	v_max3_f32 v60, v60, v22, v23
	v_max3_f32 v60, v60, v24, v25
	v_max3_f32 v60, v60, v26, v27
	v_max3_f32 v60, v60, v28, v29
	v_max3_f32 v60, v60, v30, v31
	v_max3_f32 v60, v60, v32, v33
	v_mov_b32_e32 v61, v60
	s_nop 1
	v_permlane32_swap_b32_e32 v60, v61
	v_max_f32_e32 v61, v61, v61
	v_max_f32_e32 v60, v60, v60
	v_max_f32_e32 v60, v60, v61
	v_add_f32_e32 v61, 0x7149f2ca, v60
	v_max_f32_e32 v60, 0xf149f2ca, v60
	v_cmp_ge_f32_e32 vcc, s51, v61
	v_sub_f32_e32 v61, 0xf149f2ca, v60
	v_mul_f32_e32 v61, 0x3dd53b94, v61
	v_exp_f32_e32 v61, v61
	s_cmp_eq_u64 vcc, exec
	s_cselect_b64 vcc, -1, 0
	v_cndmask_b32_e32 v208, v60, v1, vcc
	v_mul_f32_e32 v60, 0xbdd53b94, v208
	v_cndmask_b32_e64 v207, v61, 1.0, vcc
	v_mov_b32_e32 v61, v60
	v_fmac_f32_e32 v61, 0x3dd53b94, v49
	v_pk_fma_f32 v[152:153], v[18:19], s[24:25], v[60:61] op_sel_hi:[1,0,0]
	v_lshl_or_b32 v18, s67, 9, v59
	v_and_or_b32 v18, v18, s48, v57
	v_mov_b32_e32 v19, v157
	v_lshl_add_u64 v[160:161], v[18:19], 1, s[4:5]
	v_or_b32_e32 v18, s73, v54
	v_fmamk_f32 v34, v34, 0x3dd53b94, v60
	v_fmamk_f32 v35, v35, 0x3dd53b94, v60
	v_fmamk_f32 v36, v36, 0x3dd53b94, v60
	v_fmamk_f32 v37, v37, 0x3dd53b94, v60
	v_fmamk_f32 v38, v38, 0x3dd53b94, v60
	v_fmamk_f32 v39, v39, 0x3dd53b94, v60
	v_fmamk_f32 v40, v40, 0x3dd53b94, v60
	v_fmamk_f32 v41, v41, 0x3dd53b94, v60
	v_fmamk_f32 v42, v42, 0x3dd53b94, v60
	v_fmamk_f32 v43, v43, 0x3dd53b94, v60
	v_fmamk_f32 v44, v44, 0x3dd53b94, v60
	v_fmamk_f32 v45, v45, 0x3dd53b94, v60
	v_fmamk_f32 v46, v46, 0x3dd53b94, v60
	v_fmamk_f32 v47, v47, 0x3dd53b94, v60
	v_fmamk_f32 v48, v48, 0x3dd53b94, v60
	v_or3_b32 v18, v18, s74, v53
	v_exp_f32_e32 v239, v34
	v_exp_f32_e32 v241, v35
	v_exp_f32_e32 v237, v36
	v_exp_f32_e32 v240, v37
	v_exp_f32_e32 v236, v38
	v_exp_f32_e32 v238, v39
	v_exp_f32_e32 v234, v40
	v_exp_f32_e32 v235, v41
	v_exp_f32_e32 v231, v42
	v_exp_f32_e32 v233, v43
	v_exp_f32_e32 v230, v44
	v_exp_f32_e32 v232, v45
	v_exp_f32_e32 v227, v46
	v_exp_f32_e32 v229, v47
	v_exp_f32_e32 v226, v48
	v_exp_f32_e32 v228, v61
	s_or_b32 s0, s0, s66
	v_lshl_or_b32 v18, v18, 12, v56
	s_movk_i32 s4, 0x4000
	v_lshl_add_u64 v[162:163], v[18:19], 1, s[0:1]
	v_or3_b32 v18, v55, v58, s4
	v_mov_b64_e32 v[4:5], s[10:11]
	v_mov_b64_e32 v[6:7], s[12:13]
	v_mov_b64_e32 v[8:9], s[14:15]
	v_mov_b64_e32 v[10:11], s[16:17]
	v_mov_b64_e32 v[12:13], s[18:19]
	v_mov_b64_e32 v[14:15], s[20:21]
	v_pk_fma_f32 v[138:139], v[32:33], s[24:25], v[60:61] op_sel_hi:[1,0,0]
	v_pk_fma_f32 v[140:141], v[30:31], s[24:25], v[60:61] op_sel_hi:[1,0,0]
	v_pk_fma_f32 v[142:143], v[28:29], s[24:25], v[60:61] op_sel_hi:[1,0,0]
	v_pk_fma_f32 v[144:145], v[26:27], s[24:25], v[60:61] op_sel_hi:[1,0,0]
	v_pk_fma_f32 v[146:147], v[24:25], s[24:25], v[60:61] op_sel_hi:[1,0,0]
	v_pk_fma_f32 v[148:149], v[22:23], s[24:25], v[60:61] op_sel_hi:[1,0,0]
	v_pk_fma_f32 v[150:151], v[20:21], s[24:25], v[60:61] op_sel_hi:[1,0,0]
	v_lshl_add_u64 v[164:165], s[0:1], 0, v[50:51]
	v_lshl_add_u64 v[166:167], v[18:19], 1, s[0:1]
	v_mov_b64_e32 v[64:65], v[16:17]
	v_mov_b64_e32 v[48:49], v[16:17]
	v_mov_b64_e32 v[32:33], v[16:17]
	v_add_u32_e32 v181, s75, v179
	v_mov_b64_e32 v[62:63], v[14:15]
	v_mov_b64_e32 v[60:61], v[12:13]
	v_mov_b64_e32 v[58:59], v[10:11]
	v_mov_b64_e32 v[56:57], v[8:9]
	v_mov_b64_e32 v[54:55], v[6:7]
	v_mov_b64_e32 v[52:53], v[4:5]
	v_mov_b64_e32 v[50:51], v[2:3]
	v_mov_b64_e32 v[46:47], v[14:15]
	v_mov_b64_e32 v[44:45], v[12:13]
	v_mov_b64_e32 v[42:43], v[10:11]
	v_mov_b64_e32 v[40:41], v[8:9]
	v_mov_b64_e32 v[38:39], v[6:7]
	v_mov_b64_e32 v[36:37], v[4:5]
	v_mov_b64_e32 v[34:35], v[2:3]
	v_mov_b64_e32 v[30:31], v[14:15]
	v_mov_b64_e32 v[28:29], v[12:13]
	v_mov_b64_e32 v[26:27], v[10:11]
	v_mov_b64_e32 v[24:25], v[8:9]
	v_mov_b64_e32 v[22:23], v[6:7]
	v_mov_b64_e32 v[20:21], v[4:5]
	v_mov_b64_e32 v[18:19], v[2:3]
	s_mov_b32 s66, 2
.LBB0_1411:
	v_readlane_b32 s76, v254, 36
	v_readlane_b32 s77, v254, 37
	v_readlane_b32 s78, v254, 38
	v_readlane_b32 s79, v254, 39
	v_readlane_b32 s80, v254, 40
	v_readlane_b32 s81, v254, 41
	v_readlane_b32 s82, v254, 42
	v_readlane_b32 s83, v254, 43
	s_mov_b64 s[76:77], s[80:81]
	s_mov_b64 s[78:79], s[82:83]
	v_lshl_add_u64 v[170:171], s[78:79], 0, v[164:165]
	s_add_i32 s67, s33, 0
	v_lshl_add_u64 v[66:67], v[170:171], 0, s[26:27]
	s_add_i32 m0, s67, 0xc000
	v_lshl_add_u64 v[172:173], s[78:79], 0, v[166:167]
	global_load_lds_dwordx4 v[66:67], off
	v_lshl_add_u64 v[66:67], v[172:173], 0, s[26:27]
	s_add_i32 m0, s67, 0xc400
	v_lshl_add_u64 v[174:175], s[78:79], 0, v[160:161]
	s_mov_b64 s[0:1], 0xa04000
	global_load_lds_dwordx4 v[66:67], off
	v_lshl_add_u64 v[66:67], v[174:175], 0, s[0:1]
	s_add_i32 s0, s65, 0
	s_add_i32 m0, s0, 0x14000
	v_lshl_add_u64 v[168:169], s[78:79], 0, v[162:163]
	s_mov_b64 s[0:1], 0x58f00100
	global_load_lds_dwordx4 v[66:67], off
	v_lshl_add_u64 v[66:67], v[168:169], 0, s[0:1]
	s_lshl_b32 s0, s66, 14
	s_add_i32 s4, s0, s64
	s_mov_b32 m0, s4
	s_mov_b64 s[0:1], 0x58f00180
	global_load_lds_dwordx4 v[66:67], off
	v_lshl_add_u64 v[66:67], v[168:169], 0, s[0:1]
	s_add_i32 m0, s4, 0x400
	s_nop 0
	global_load_lds_dwordx4 v[66:67], off
	v_add_u32_e32 v209, s52, v182
	ds_read_b128 v[66:69], v209
	ds_read_b128 v[70:73], v209 offset:8192
	v_add_u32_e32 v210, s52, v184
	ds_read_b128 v[212:215], v210
	ds_read_b128 v[216:219], v210 offset:8192
	v_add_u32_e32 v211, s52, v186
	s_waitcnt lgkmcnt(0)
	v_mfma_f32_32x32x16_bf16 v[82:97], v[66:69], v[134:137], 0
	v_exp_f32_e32 v152, v152
	v_exp_f32_e32 v153, v153
	v_exp_f32_e32 v225, v150
	v_exp_f32_e32 v151, v151
	v_exp_f32_e32 v148, v148
	v_exp_f32_e32 v149, v149
	v_exp_f32_e32 v146, v146
	v_mfma_f32_32x32x16_bf16 v[66:81], v[70:73], v[134:137], 0
	v_exp_f32_e32 v147, v147
	v_mfma_f32_32x32x16_bf16 v[66:81], v[216:219], v[130:133], v[66:81]
	v_mfma_f32_32x32x16_bf16 v[82:97], v[212:215], v[130:133], v[82:97]
	ds_read_b128 v[212:215], v211
	ds_read_b128 v[216:219], v211 offset:8192
	s_waitcnt lgkmcnt(0)
	v_mfma_f32_32x32x16_bf16 v[66:81], v[216:219], v[126:129], v[66:81]
	v_mfma_f32_32x32x16_bf16 v[82:97], v[212:215], v[126:129], v[82:97]
	v_add_u32_e32 v212, s52, v188
	ds_read_b128 v[214:217], v212
	ds_read_b128 v[218:221], v212 offset:8192
	v_add_u32_e32 v213, s52, v190
	s_waitcnt lgkmcnt(0)
	v_mfma_f32_32x32x16_bf16 v[66:81], v[218:221], v[122:125], v[66:81]
	v_mfma_f32_32x32x16_bf16 v[82:97], v[214:217], v[122:125], v[82:97]
	ds_read_b128 v[214:217], v213
	ds_read_b128 v[218:221], v213 offset:8192
	s_waitcnt lgkmcnt(0)
	v_mfma_f32_32x32x16_bf16 v[66:81], v[218:221], v[118:121], v[66:81]
	v_mfma_f32_32x32x16_bf16 v[82:97], v[214:217], v[118:121], v[82:97]
	v_add_u32_e32 v214, s52, v192
	ds_read_b128 v[216:219], v214
	ds_read_b128 v[242:245], v214 offset:8192
	v_add_u32_e32 v215, s52, v194
	s_waitcnt lgkmcnt(0)
	v_mfma_f32_32x32x16_bf16 v[66:81], v[242:245], v[114:117], v[66:81]
	v_mfma_f32_32x32x16_bf16 v[82:97], v[216:219], v[114:117], v[82:97]
	ds_read_b128 v[216:219], v215
	ds_read_b128 v[242:245], v215 offset:8192
	s_waitcnt lgkmcnt(0)
	v_mfma_f32_32x32x16_bf16 v[66:81], v[242:245], v[110:113], v[66:81]
	v_mfma_f32_32x32x16_bf16 v[82:97], v[216:219], v[110:113], v[82:97]
	v_add_u32_e32 v216, s52, v196
	ds_read_b128 v[218:221], v216
	ds_read_b128 v[242:245], v216 offset:8192
	v_add_u32_e32 v217, s53, v199
	s_waitcnt lgkmcnt(0)
	v_mfma_f32_32x32x16_bf16 v[66:81], v[242:245], v[106:109], v[66:81]
	v_mfma_f32_32x32x16_bf16 v[82:97], v[218:221], v[106:109], v[82:97]
	ds_read_b128 v[218:221], v217
	ds_read_b128 v[242:245], v217 offset:4096
	s_waitcnt lgkmcnt(0)
	v_mfma_f32_32x32x16_bf16 v[66:81], v[242:245], v[102:105], v[66:81]
	v_mfma_f32_32x32x16_bf16 v[82:97], v[218:221], v[102:105], v[82:97]
	v_add_u32_e32 v218, s53, v201
	ds_read_b128 v[242:245], v218
	ds_read_b128 v[246:249], v218 offset:4096
	v_add_u32_e32 v219, s53, v203
	v_add_u32_e32 v220, s53, v205
	s_waitcnt lgkmcnt(0)
	v_mfma_f32_32x32x16_bf16 v[66:81], v[246:249], v[98:101], v[66:81]
	v_mfma_f32_32x32x16_bf16 v[82:97], v[242:245], v[98:101], v[82:97]
	ds_read_b128 v[242:245], v219
	ds_read_b128 v[246:249], v219 offset:4096
	ds_read_b128 v[250:253], v180
	s_waitcnt lgkmcnt(0)
	v_mfma_f32_32x32x16_bf16 v[66:81], v[246:249], v[250:253], v[66:81]
	v_mfma_f32_32x32x16_bf16 v[82:97], v[242:245], v[250:253], v[82:97]
	ds_read_b128 v[242:245], v220
	ds_read_b128 v[246:249], v220 offset:4096
	ds_read_b128 v[250:253], v180 offset:1024
	s_waitcnt lgkmcnt(0)
	v_mfma_f32_32x32x16_bf16 v[66:81], v[246:249], v[250:253], v[66:81]
	v_exp_f32_e32 v248, v138
	v_add_f32_e32 v138, 0, v239
	v_add_f32_e32 v138, v241, v138
	v_add_f32_e32 v138, v237, v138
	v_add_f32_e32 v138, v240, v138
	v_add_f32_e32 v138, v236, v138
	v_add_f32_e32 v138, v238, v138
	v_add_f32_e32 v138, v234, v138
	v_add_f32_e32 v138, v235, v138
	v_add_f32_e32 v138, v231, v138
	v_add_f32_e32 v138, v233, v138
	v_add_f32_e32 v138, v230, v138
	v_add_f32_e32 v138, v232, v138
	v_add_f32_e32 v138, v227, v138
	v_add_f32_e32 v138, v229, v138
	v_add_f32_e32 v138, v226, v138
	v_add_f32_e32 v138, v228, v138
	v_add_f32_e32 v138, v152, v138
	v_add_f32_e32 v138, v153, v138
	v_add_f32_e32 v138, v225, v138
	v_add_f32_e32 v138, v151, v138
	v_mfma_f32_32x32x16_bf16 v[82:97], v[242:245], v[250:253], v[82:97]
	v_exp_f32_e32 v242, v144
	v_add_f32_e32 v138, v148, v138
	v_exp_f32_e32 v243, v145
	v_add_f32_e32 v138, v149, v138
	v_exp_f32_e32 v244, v142
	v_add_f32_e32 v138, v146, v138
	v_exp_f32_e32 v245, v143
	v_add_f32_e32 v138, v147, v138
	v_exp_f32_e32 v246, v140
	v_add_f32_e32 v138, v242, v138
	v_exp_f32_e32 v247, v141
	v_add_f32_e32 v138, v243, v138
	v_add_f32_e32 v138, v244, v138
	v_exp_f32_e32 v249, v139
	v_add_f32_e32 v138, v245, v138
	v_add_f32_e32 v138, v246, v138
	v_add_f32_e32 v138, v247, v138
	v_add_f32_e32 v138, v248, v138
	v_add_f32_e32 v221, v249, v138
	v_mov_b32_e32 v224, v221
	v_cvt_pk_bf16_f32 v138, v239, v241
	v_cvt_pk_bf16_f32 v139, v237, v240
	v_cvt_pk_bf16_f32 v140, v236, v238
	s_nop 1
	v_permlane32_swap_b32_e32 v221, v224
	v_cvt_pk_bf16_f32 v141, v234, v235
	v_permlane32_swap_b32_e32 v138, v140
	v_cvt_pk_bf16_f32 v142, v231, v233
	v_cvt_pk_bf16_f32 v143, v230, v232
	v_cvt_pk_bf16_f32 v144, v227, v229
	v_cvt_pk_bf16_f32 v145, v226, v228
	v_cvt_pk_bf16_f32 v150, v152, v153
	v_cvt_pk_bf16_f32 v151, v225, v151
	v_cvt_pk_bf16_f32 v152, v148, v149
	v_cvt_pk_bf16_f32 v153, v146, v147
	v_cvt_pk_bf16_f32 v146, v242, v243
	v_cvt_pk_bf16_f32 v147, v244, v245
	v_cvt_pk_bf16_f32 v148, v246, v247
	v_cvt_pk_bf16_f32 v149, v248, v249
	v_permlane32_swap_b32_e32 v139, v141
	v_permlane32_swap_b32_e32 v142, v144
	v_permlane32_swap_b32_e32 v143, v145
	v_permlane32_swap_b32_e32 v150, v152
	v_permlane32_swap_b32_e32 v151, v153
	v_permlane32_swap_b32_e32 v146, v148
	v_permlane32_swap_b32_e32 v147, v149
	v_lshl_add_u32 v225, s37, 14, v181
	ds_read_b64_tr_b16 v[226:227], v225 offset:0
	ds_read_b64_tr_b16 v[228:229], v225 offset:0x800
	ds_read_b64_tr_b16 v[230:231], v225 offset:0x1000
	ds_read_b64_tr_b16 v[232:233], v225 offset:0x1800
	ds_read_b64_tr_b16 v[234:235], v225 offset:0x2000
	ds_read_b64_tr_b16 v[236:237], v225 offset:0x2800
	ds_read_b64_tr_b16 v[238:239], v225 offset:0x3000
	ds_read_b64_tr_b16 v[240:241], v225 offset:0x3800
	s_waitcnt lgkmcnt(0)
	s_nop 0
	v_mfma_f32_32x32x16_bf16 v[2:17], v[138:141], v[226:229], v[2:17]
	ds_read_b64_tr_b16 v[226:227], v225 offset:0x200
	ds_read_b64_tr_b16 v[228:229], v225 offset:0xa00
	v_mfma_f32_32x32x16_bf16 v[2:17], v[142:145], v[230:233], v[2:17]
	ds_read_b64_tr_b16 v[230:231], v225 offset:0x1200
	ds_read_b64_tr_b16 v[232:233], v225 offset:0x1a00
	v_mfma_f32_32x32x16_bf16 v[2:17], v[150:153], v[234:237], v[2:17]
	ds_read_b64_tr_b16 v[234:235], v225 offset:0x2200
	ds_read_b64_tr_b16 v[236:237], v225 offset:0x2a00
	ds_read_b64_tr_b16 v[242:243], v225 offset:0x3200
	ds_read_b64_tr_b16 v[244:245], v225 offset:0x3a00
	v_mfma_f32_32x32x16_bf16 v[2:17], v[146:149], v[238:241], v[2:17]
	s_waitcnt lgkmcnt(6)
	v_mfma_f32_32x32x16_bf16 v[50:65], v[138:141], v[226:229], v[50:65]
	ds_read_b64_tr_b16 v[226:227], v225 offset:0x400
	ds_read_b64_tr_b16 v[228:229], v225 offset:0xc00
	s_waitcnt lgkmcnt(6)
	v_mfma_f32_32x32x16_bf16 v[50:65], v[142:145], v[230:233], v[50:65]
	ds_read_b64_tr_b16 v[230:231], v225 offset:0x1400
	ds_read_b64_tr_b16 v[232:233], v225 offset:0x1c00
	s_waitcnt lgkmcnt(6)
	v_mfma_f32_32x32x16_bf16 v[50:65], v[150:153], v[234:237], v[50:65]
	ds_read_b64_tr_b16 v[234:235], v225 offset:0x2400
	ds_read_b64_tr_b16 v[236:237], v225 offset:0x2c00
	ds_read_b64_tr_b16 v[238:239], v225 offset:0x3400
	ds_read_b64_tr_b16 v[240:241], v225 offset:0x3c00
	s_waitcnt lgkmcnt(8)
	v_mfma_f32_32x32x16_bf16 v[50:65], v[146:149], v[242:245], v[50:65]
	s_waitcnt lgkmcnt(6)
	v_mfma_f32_32x32x16_bf16 v[34:49], v[138:141], v[226:229], v[34:49]
	ds_read_b64_tr_b16 v[226:227], v225 offset:0x600
	ds_read_b64_tr_b16 v[228:229], v225 offset:0xe00
	s_waitcnt lgkmcnt(6)
	v_mfma_f32_32x32x16_bf16 v[34:49], v[142:145], v[230:233], v[34:49]
	ds_read_b64_tr_b16 v[230:231], v225 offset:0x1600
	ds_read_b64_tr_b16 v[232:233], v225 offset:0x1e00
	s_waitcnt lgkmcnt(6)
	v_mfma_f32_32x32x16_bf16 v[34:49], v[150:153], v[234:237], v[34:49]
	ds_read_b64_tr_b16 v[234:235], v225 offset:0x2600
	ds_read_b64_tr_b16 v[236:237], v225 offset:0x2e00
	ds_read_b64_tr_b16 v[242:243], v225 offset:0x3600
	ds_read_b64_tr_b16 v[244:245], v225 offset:0x3e00
	s_waitcnt lgkmcnt(8)
	v_mfma_f32_32x32x16_bf16 v[34:49], v[146:149], v[238:241], v[34:49]
	s_waitcnt lgkmcnt(6)
	v_mfma_f32_32x32x16_bf16 v[18:33], v[138:141], v[226:229], v[18:33]
	v_max_f32_e32 v225, v83, v83
	v_max_f32_e32 v238, v82, v82
	v_max_f32_e32 v225, v238, v225
	v_max3_f32 v225, v225, v84, v85
	v_max3_f32 v225, v225, v86, v87
	v_max3_f32 v138, v225, v88, v89
	v_max3_f32 v138, v138, v90, v91
	v_max3_f32 v138, v138, v92, v93
	s_waitcnt lgkmcnt(4)
	v_mfma_f32_32x32x16_bf16 v[18:33], v[142:145], v[230:233], v[18:33]
	v_max3_f32 v138, v138, v94, v95
	v_max3_f32 v138, v138, v96, v97
	v_max3_f32 v138, v138, v66, v67
	v_max3_f32 v138, v138, v68, v69
	v_max3_f32 v138, v138, v70, v71
	v_max3_f32 v138, v138, v72, v73
	v_max3_f32 v138, v138, v74, v75
	v_max3_f32 v138, v138, v76, v77
	s_waitcnt lgkmcnt(2)
	v_mfma_f32_32x32x16_bf16 v[18:33], v[150:153], v[234:237], v[18:33]
	v_max3_f32 v138, v138, v78, v79
	v_max3_f32 v138, v138, v80, v81
	v_mov_b32_e32 v139, v138
	s_nop 1
	v_permlane32_swap_b32_e32 v138, v139
	v_max_f32_e32 v139, v139, v139
	v_max_f32_e32 v138, v138, v138
	v_max_f32_e32 v138, v138, v139
	v_max_f32_e32 v140, v208, v208
	v_sub_f32_e32 v139, v138, v208
	v_max_f32_e32 v138, v140, v138
	s_waitcnt lgkmcnt(0)
	v_mfma_f32_32x32x16_bf16 v[18:33], v[146:149], v[242:245], v[18:33]
	v_sub_f32_e32 v140, v208, v138
	v_mul_f32_e32 v140, 0x3dd53b94, v140
	v_exp_f32_e32 v140, v140
	v_cmp_ge_f32_e32 vcc, s51, v139
	s_cmp_eq_u64 vcc, exec
	s_cselect_b64 s[4:5], -1, 0
	v_cndmask_b32_e64 v225, v140, 1.0, s[4:5]
	v_cmp_gt_f32_e32 vcc, 1.0, v225
	s_cbranch_vccz .LBB0_1415
	s_and_saveexec_b64 s[0:1], s[2:3]
	ds_write_b32 v177, v225 offset:128
	s_or_b64 exec, exec, s[0:1]
	s_waitcnt lgkmcnt(0)
	v_add_u32_e32 v139, v159, v156
	ds_read_b128 v[140:143], v139 offset:224
	ds_read_b128 v[144:147], v139 offset:192
	ds_read_b128 v[148:151], v139 offset:160
	ds_read_b128 v[226:229], v139 offset:128
	s_waitcnt lgkmcnt(0)
	v_pk_mul_f32 v[14:15], v[14:15], v[140:141]
	v_pk_mul_f32 v[10:11], v[10:11], v[144:145]
	v_pk_mul_f32 v[6:7], v[6:7], v[148:149]
	v_pk_mul_f32 v[16:17], v[16:17], v[142:143]
	v_pk_mul_f32 v[12:13], v[12:13], v[146:147]
	v_pk_mul_f32 v[8:9], v[8:9], v[150:151]
	v_pk_mul_f32 v[4:5], v[4:5], v[228:229]
	v_pk_mul_f32 v[2:3], v[2:3], v[226:227]
	v_pk_mul_f32 v[62:63], v[62:63], v[140:141]
	v_pk_mul_f32 v[58:59], v[58:59], v[144:145]
	v_pk_mul_f32 v[54:55], v[54:55], v[148:149]
	v_pk_mul_f32 v[64:65], v[64:65], v[142:143]
	v_pk_mul_f32 v[60:61], v[60:61], v[146:147]
	v_pk_mul_f32 v[56:57], v[56:57], v[150:151]
	v_pk_mul_f32 v[52:53], v[52:53], v[228:229]
	v_pk_mul_f32 v[50:51], v[50:51], v[226:227]
	v_pk_mul_f32 v[46:47], v[46:47], v[140:141]
	v_pk_mul_f32 v[42:43], v[42:43], v[144:145]
	v_pk_mul_f32 v[38:39], v[38:39], v[148:149]
	v_pk_mul_f32 v[48:49], v[48:49], v[142:143]
	v_pk_mul_f32 v[44:45], v[44:45], v[146:147]
	v_pk_mul_f32 v[40:41], v[40:41], v[150:151]
	v_pk_mul_f32 v[36:37], v[36:37], v[228:229]
	v_pk_mul_f32 v[34:35], v[34:35], v[226:227]
	v_pk_mul_f32 v[30:31], v[30:31], v[140:141]
	v_pk_mul_f32 v[26:27], v[26:27], v[144:145]
	v_pk_mul_f32 v[22:23], v[22:23], v[148:149]
	v_pk_mul_f32 v[32:33], v[32:33], v[142:143]
	v_pk_mul_f32 v[28:29], v[28:29], v[146:147]
	v_pk_mul_f32 v[24:25], v[24:25], v[150:151]
	v_pk_mul_f32 v[20:21], v[20:21], v[228:229]
	v_pk_mul_f32 v[18:19], v[18:19], v[226:227]
.LBB0_1415:
	s_add_i32 s0, s37, 1
	s_cmp_lg_u32 s37, 2
	s_cselect_b32 s37, s0, 0
	s_add_i32 s0, s66, 1
	s_cmp_lg_u32 s66, 2
	s_cselect_b32 s66, s0, 0
	v_lshl_add_u64 v[140:141], v[170:171], 0, s[28:29]
	s_add_i32 m0, s67, 0x10000
	s_waitcnt vmcnt(2)
	s_waitcnt vmcnt(0)
	s_barrier
	global_load_lds_dwordx4 v[140:141], off
	v_lshl_add_u64 v[140:141], v[172:173], 0, s[28:29]
	s_add_i32 m0, s67, 0x10400
	s_mov_b64 s[0:1], 0xa06000
	global_load_lds_dwordx4 v[140:141], off
	v_lshl_add_u64 v[140:141], v[174:175], 0, s[0:1]
	s_add_i32 s0, s50, s65
	s_add_i32 m0, s0, 0x2000
	s_mov_b64 s[0:1], 0x58f80100
	global_load_lds_dwordx4 v[140:141], off
	v_lshl_add_u64 v[140:141], v[168:169], 0, s[0:1]
	s_lshl_b32 s0, s66, 14
	s_add_i32 s67, s0, s64
	s_mov_b32 m0, s67
	s_mov_b64 s[0:1], 0x58f80180
	global_load_lds_dwordx4 v[140:141], off
	v_lshl_add_u64 v[140:141], v[168:169], 0, s[0:1]
	s_add_i32 m0, s67, 0x400
	v_cndmask_b32_e64 v169, v138, v208, s[4:5]
	global_load_lds_dwordx4 v[140:141], off
	v_mul_f32_e32 v150, 0xbdd53b94, v169
	v_fmamk_f32 v82, v82, 0x3dd53b94, v150
	v_fmamk_f32 v83, v83, 0x3dd53b94, v150
	v_fmamk_f32 v84, v84, 0x3dd53b94, v150
	v_fmamk_f32 v85, v85, 0x3dd53b94, v150
	v_fmamk_f32 v86, v86, 0x3dd53b94, v150
	v_fmamk_f32 v87, v87, 0x3dd53b94, v150
	v_fmamk_f32 v88, v88, 0x3dd53b94, v150
	v_fmamk_f32 v89, v89, 0x3dd53b94, v150
	v_fmamk_f32 v90, v90, 0x3dd53b94, v150
	v_fmamk_f32 v91, v91, 0x3dd53b94, v150
	v_fmamk_f32 v92, v92, 0x3dd53b94, v150
	v_fmamk_f32 v93, v93, 0x3dd53b94, v150
	v_fmamk_f32 v94, v94, 0x3dd53b94, v150
	v_fmamk_f32 v95, v95, 0x3dd53b94, v150
	v_fmamk_f32 v96, v96, 0x3dd53b94, v150
	v_fmamk_f32 v97, v97, 0x3dd53b94, v150
	v_fmamk_f32 v168, v69, 0x3dd53b94, v150
	v_fmamk_f32 v170, v70, 0x3dd53b94, v150
	v_fmamk_f32 v171, v71, 0x3dd53b94, v150
	v_fmamk_f32 v151, v66, 0x3dd53b94, v150
	v_fmamk_f32 v152, v67, 0x3dd53b94, v150
	v_fmamk_f32 v153, v68, 0x3dd53b94, v150
	v_fmamk_f32 v172, v72, 0x3dd53b94, v150
	v_fmamk_f32 v173, v73, 0x3dd53b94, v150
	v_fmamk_f32 v174, v74, 0x3dd53b94, v150
	v_fmamk_f32 v175, v75, 0x3dd53b94, v150
	v_fmamk_f32 v208, v76, 0x3dd53b94, v150
	v_fmamk_f32 v226, v77, 0x3dd53b94, v150
	v_fmamk_f32 v227, v78, 0x3dd53b94, v150
	v_exp_f32_e32 v228, v82
	v_exp_f32_e32 v229, v83
	v_exp_f32_e32 v230, v84
	v_exp_f32_e32 v231, v85
	v_exp_f32_e32 v232, v86
	v_exp_f32_e32 v233, v87
	v_exp_f32_e32 v234, v88
	v_exp_f32_e32 v235, v89
	v_exp_f32_e32 v236, v90
	v_exp_f32_e32 v237, v91
	v_exp_f32_e32 v238, v92
	v_exp_f32_e32 v239, v93
	v_exp_f32_e32 v240, v94
	v_exp_f32_e32 v241, v95
	v_exp_f32_e32 v242, v96
	v_exp_f32_e32 v243, v97
	v_fmamk_f32 v244, v79, 0x3dd53b94, v150
	v_fmamk_f32 v245, v80, 0x3dd53b94, v150
	v_fmac_f32_e32 v150, 0x3dd53b94, v81
	ds_read_b128 v[66:69], v183 offset:49152
	ds_read_b128 v[70:73], v183 offset:57344
	ds_read_b128 v[138:141], v185 offset:49152
	ds_read_b128 v[142:145], v185 offset:57344
	s_waitcnt lgkmcnt(0)
	v_mfma_f32_32x32x16_bf16 v[82:97], v[66:69], v[134:137], 0
	v_mfma_f32_32x32x16_bf16 v[66:81], v[70:73], v[134:137], 0
	v_mfma_f32_32x32x16_bf16 v[82:97], v[138:141], v[130:133], v[82:97]
	v_mfma_f32_32x32x16_bf16 v[66:81], v[142:145], v[130:133], v[66:81]
	ds_read_b128 v[138:141], v187 offset:49152
	ds_read_b128 v[142:145], v187 offset:57344
	s_waitcnt lgkmcnt(0)
	v_mfma_f32_32x32x16_bf16 v[82:97], v[138:141], v[126:129], v[82:97]
	v_mfma_f32_32x32x16_bf16 v[66:81], v[142:145], v[126:129], v[66:81]
	ds_read_b128 v[138:141], v189 offset:49152
	ds_read_b128 v[142:145], v189 offset:57344
	s_waitcnt lgkmcnt(0)
	v_mfma_f32_32x32x16_bf16 v[82:97], v[138:141], v[122:125], v[82:97]
	v_mfma_f32_32x32x16_bf16 v[66:81], v[142:145], v[122:125], v[66:81]
	ds_read_b128 v[138:141], v191 offset:49152
	ds_read_b128 v[142:145], v191 offset:57344
	s_waitcnt lgkmcnt(0)
	v_mfma_f32_32x32x16_bf16 v[82:97], v[138:141], v[118:121], v[82:97]
	v_mfma_f32_32x32x16_bf16 v[66:81], v[142:145], v[118:121], v[66:81]
	ds_read_b128 v[138:141], v193 offset:49152
	ds_read_b128 v[142:145], v193 offset:57344
	s_waitcnt lgkmcnt(0)
	v_mfma_f32_32x32x16_bf16 v[82:97], v[138:141], v[114:117], v[82:97]
	v_mfma_f32_32x32x16_bf16 v[66:81], v[142:145], v[114:117], v[66:81]
	ds_read_b128 v[138:141], v195 offset:49152
	ds_read_b128 v[142:145], v195 offset:57344
	s_waitcnt lgkmcnt(0)
	v_mfma_f32_32x32x16_bf16 v[82:97], v[138:141], v[110:113], v[82:97]
	v_mfma_f32_32x32x16_bf16 v[66:81], v[142:145], v[110:113], v[66:81]
	ds_read_b128 v[138:141], v197 offset:49152
	ds_read_b128 v[142:145], v197 offset:57344
	s_waitcnt lgkmcnt(0)
	v_mfma_f32_32x32x16_bf16 v[82:97], v[138:141], v[106:109], v[82:97]
	v_mfma_f32_32x32x16_bf16 v[66:81], v[142:145], v[106:109], v[66:81]
	ds_read_b128 v[138:141], v200
	ds_read_b128 v[142:145], v200 offset:4096
	s_waitcnt lgkmcnt(0)
	v_mfma_f32_32x32x16_bf16 v[82:97], v[138:141], v[102:105], v[82:97]
	v_mfma_f32_32x32x16_bf16 v[66:81], v[142:145], v[102:105], v[66:81]
	ds_read_b128 v[138:141], v202
	ds_read_b128 v[142:145], v202 offset:4096
	s_waitcnt lgkmcnt(0)
	v_mfma_f32_32x32x16_bf16 v[82:97], v[138:141], v[98:101], v[82:97]
	v_mfma_f32_32x32x16_bf16 v[66:81], v[142:145], v[98:101], v[66:81]
	ds_read_b128 v[138:141], v204
	ds_read_b128 v[142:145], v204 offset:4096
	ds_read_b128 v[146:149], v180
	s_waitcnt lgkmcnt(0)
	v_mfma_f32_32x32x16_bf16 v[82:97], v[138:141], v[146:149], v[82:97]
	v_mfma_f32_32x32x16_bf16 v[66:81], v[142:145], v[146:149], v[66:81]
	ds_read_b128 v[138:141], v206
	ds_read_b128 v[142:145], v206 offset:4096
	ds_read_b128 v[146:149], v180 offset:1024
	s_waitcnt lgkmcnt(0)
	v_mfma_f32_32x32x16_bf16 v[82:97], v[138:141], v[146:149], v[82:97]
	v_add_f32_e32 v138, 0, v228
	v_add_f32_e32 v138, v229, v138
	v_add_f32_e32 v138, v230, v138
	v_add_f32_e32 v138, v231, v138
	v_add_f32_e32 v138, v232, v138
	v_add_f32_e32 v138, v233, v138
	v_add_f32_e32 v138, v234, v138
	v_add_f32_e32 v138, v235, v138
	v_add_f32_e32 v138, v236, v138
	v_add_f32_e32 v138, v237, v138
	v_add_f32_e32 v138, v238, v138
	v_add_f32_e32 v138, v239, v138
	v_mfma_f32_32x32x16_bf16 v[66:81], v[142:145], v[146:149], v[66:81]
	v_exp_f32_e32 v146, v151
	v_add_f32_e32 v138, v240, v138
	v_exp_f32_e32 v147, v152
	v_add_f32_e32 v138, v241, v138
	v_exp_f32_e32 v148, v153
	v_add_f32_e32 v138, v242, v138
	v_exp_f32_e32 v149, v168
	v_add_f32_e32 v138, v243, v138
	v_exp_f32_e32 v152, v170
	v_add_f32_e32 v138, v146, v138
	v_exp_f32_e32 v153, v171
	v_add_f32_e32 v138, v147, v138
	v_exp_f32_e32 v168, v172
	v_add_f32_e32 v138, v148, v138
	v_exp_f32_e32 v172, v173
	v_add_f32_e32 v138, v149, v138
	v_exp_f32_e32 v173, v174
	v_add_f32_e32 v138, v152, v138
	v_exp_f32_e32 v174, v175
	v_add_f32_e32 v138, v153, v138
	v_exp_f32_e32 v175, v208
	v_add_f32_e32 v138, v168, v138
	v_exp_f32_e32 v208, v226
	v_add_f32_e32 v138, v172, v138
	v_exp_f32_e32 v226, v227
	v_add_f32_e32 v138, v173, v138
	v_exp_f32_e32 v227, v244
	v_add_f32_e32 v138, v174, v138
	v_exp_f32_e32 v244, v245
	v_add_f32_e32 v138, v175, v138
	v_exp_f32_e32 v245, v150
	v_add_f32_e32 v138, v208, v138
	v_add_f32_e32 v138, v226, v138
	v_add_f32_e32 v138, v227, v138
	v_add_f32_e32 v138, v244, v138
	v_add_f32_e32 v170, v245, v138
	v_mov_b32_e32 v171, v170
	v_cvt_pk_bf16_f32 v138, v228, v229
	v_cvt_pk_bf16_f32 v139, v230, v231
	v_cvt_pk_bf16_f32 v140, v232, v233
	s_nop 1
	v_permlane32_swap_b32_e32 v170, v171
	v_cvt_pk_bf16_f32 v141, v234, v235
	v_permlane32_swap_b32_e32 v138, v140
	v_cvt_pk_bf16_f32 v142, v236, v237
	v_cvt_pk_bf16_f32 v143, v238, v239
	v_cvt_pk_bf16_f32 v144, v240, v241
	v_cvt_pk_bf16_f32 v145, v242, v243
	v_cvt_pk_bf16_f32 v150, v146, v147
	v_cvt_pk_bf16_f32 v151, v148, v149
	v_cvt_pk_bf16_f32 v152, v152, v153
	v_cvt_pk_bf16_f32 v153, v168, v172
	v_cvt_pk_bf16_f32 v146, v173, v174
	v_cvt_pk_bf16_f32 v147, v175, v208
	v_cvt_pk_bf16_f32 v148, v226, v227
	v_cvt_pk_bf16_f32 v149, v244, v245
	v_permlane32_swap_b32_e32 v139, v141
	v_permlane32_swap_b32_e32 v142, v144
	v_permlane32_swap_b32_e32 v143, v145
	v_permlane32_swap_b32_e32 v150, v152
	v_permlane32_swap_b32_e32 v151, v153
	v_permlane32_swap_b32_e32 v146, v148
	v_permlane32_swap_b32_e32 v147, v149
	v_lshl_add_u32 v168, s37, 14, v181
	ds_read_b64_tr_b16 v[172:173], v168 offset:0
	ds_read_b64_tr_b16 v[174:175], v168 offset:0x800
	ds_read_b64_tr_b16 v[226:227], v168 offset:0x1000
	ds_read_b64_tr_b16 v[228:229], v168 offset:0x1800
	ds_read_b64_tr_b16 v[230:231], v168 offset:0x2000
	ds_read_b64_tr_b16 v[232:233], v168 offset:0x2800
	ds_read_b64_tr_b16 v[234:235], v168 offset:0x3000
	ds_read_b64_tr_b16 v[236:237], v168 offset:0x3800
	s_waitcnt lgkmcnt(0)
	s_nop 0
	v_mfma_f32_32x32x16_bf16 v[2:17], v[138:141], v[172:175], v[2:17]
	ds_read_b64_tr_b16 v[172:173], v168 offset:0x200
	ds_read_b64_tr_b16 v[174:175], v168 offset:0xa00
	v_mfma_f32_32x32x16_bf16 v[2:17], v[142:145], v[226:229], v[2:17]
	ds_read_b64_tr_b16 v[226:227], v168 offset:0x1200
	ds_read_b64_tr_b16 v[228:229], v168 offset:0x1a00
	v_mfma_f32_32x32x16_bf16 v[2:17], v[150:153], v[230:233], v[2:17]
	ds_read_b64_tr_b16 v[230:231], v168 offset:0x2200
	ds_read_b64_tr_b16 v[232:233], v168 offset:0x2a00
	ds_read_b64_tr_b16 v[238:239], v168 offset:0x3200
	ds_read_b64_tr_b16 v[240:241], v168 offset:0x3a00
	v_mfma_f32_32x32x16_bf16 v[2:17], v[146:149], v[234:237], v[2:17]
	s_waitcnt lgkmcnt(6)
	v_mfma_f32_32x32x16_bf16 v[50:65], v[138:141], v[172:175], v[50:65]
	ds_read_b64_tr_b16 v[172:173], v168 offset:0x400
	ds_read_b64_tr_b16 v[174:175], v168 offset:0xc00
	s_waitcnt lgkmcnt(6)
	v_mfma_f32_32x32x16_bf16 v[50:65], v[142:145], v[226:229], v[50:65]
	ds_read_b64_tr_b16 v[226:227], v168 offset:0x1400
	ds_read_b64_tr_b16 v[228:229], v168 offset:0x1c00
	s_waitcnt lgkmcnt(6)
	v_mfma_f32_32x32x16_bf16 v[50:65], v[150:153], v[230:233], v[50:65]
	ds_read_b64_tr_b16 v[230:231], v168 offset:0x2400
	ds_read_b64_tr_b16 v[232:233], v168 offset:0x2c00
	ds_read_b64_tr_b16 v[234:235], v168 offset:0x3400
	ds_read_b64_tr_b16 v[236:237], v168 offset:0x3c00
	s_waitcnt lgkmcnt(8)
	v_mfma_f32_32x32x16_bf16 v[50:65], v[146:149], v[238:241], v[50:65]
	s_waitcnt lgkmcnt(6)
	v_mfma_f32_32x32x16_bf16 v[34:49], v[138:141], v[172:175], v[34:49]
	ds_read_b64_tr_b16 v[172:173], v168 offset:0x600
	ds_read_b64_tr_b16 v[174:175], v168 offset:0xe00
	s_waitcnt lgkmcnt(6)
	v_mfma_f32_32x32x16_bf16 v[34:49], v[142:145], v[226:229], v[34:49]
	ds_read_b64_tr_b16 v[226:227], v168 offset:0x1600
	ds_read_b64_tr_b16 v[228:229], v168 offset:0x1e00
	s_waitcnt lgkmcnt(6)
	v_mfma_f32_32x32x16_bf16 v[34:49], v[150:153], v[230:233], v[34:49]
	ds_read_b64_tr_b16 v[230:231], v168 offset:0x2600
	ds_read_b64_tr_b16 v[232:233], v168 offset:0x2e00
	ds_read_b64_tr_b16 v[238:239], v168 offset:0x3600
	ds_read_b64_tr_b16 v[240:241], v168 offset:0x3e00
	s_waitcnt lgkmcnt(8)
	v_mfma_f32_32x32x16_bf16 v[34:49], v[146:149], v[234:237], v[34:49]
	s_waitcnt lgkmcnt(6)
	v_mfma_f32_32x32x16_bf16 v[18:33], v[138:141], v[172:175], v[18:33]
	v_max_f32_e32 v168, v83, v83
	v_max_f32_e32 v208, v82, v82
	v_max_f32_e32 v168, v208, v168
	v_max3_f32 v168, v168, v84, v85
	v_max3_f32 v168, v168, v86, v87
	v_max3_f32 v138, v168, v88, v89
	v_max3_f32 v138, v138, v90, v91
	v_max3_f32 v138, v138, v92, v93
	s_waitcnt lgkmcnt(4)
	v_mfma_f32_32x32x16_bf16 v[18:33], v[142:145], v[226:229], v[18:33]
	v_max3_f32 v138, v138, v94, v95
	v_max3_f32 v138, v138, v96, v97
	v_max3_f32 v138, v138, v66, v67
	v_max3_f32 v138, v138, v68, v69
	v_max3_f32 v138, v138, v70, v71
	v_max3_f32 v138, v138, v72, v73
	v_max3_f32 v138, v138, v74, v75
	v_max3_f32 v138, v138, v76, v77
	s_waitcnt lgkmcnt(2)
	v_mfma_f32_32x32x16_bf16 v[18:33], v[150:153], v[230:233], v[18:33]
	v_max3_f32 v138, v138, v78, v79
	v_max3_f32 v138, v138, v80, v81
	v_mov_b32_e32 v139, v138
	s_nop 1
	v_permlane32_swap_b32_e32 v138, v139
	v_max_f32_e32 v139, v139, v139
	v_max_f32_e32 v138, v138, v138
	v_max_f32_e32 v138, v138, v139
	v_max_f32_e32 v140, v169, v169
	v_sub_f32_e32 v139, v138, v169
	v_max_f32_e32 v138, v140, v138
	s_waitcnt lgkmcnt(0)
	v_mfma_f32_32x32x16_bf16 v[18:33], v[146:149], v[238:241], v[18:33]
	v_sub_f32_e32 v140, v169, v138
	v_mul_f32_e32 v140, 0x3dd53b94, v140
	v_exp_f32_e32 v140, v140
	v_cmp_ge_f32_e32 vcc, s51, v139
	s_cmp_eq_u64 vcc, exec
	s_cselect_b64 s[4:5], -1, 0
	v_cndmask_b32_e64 v168, v140, 1.0, s[4:5]
	v_cmp_gt_f32_e32 vcc, 1.0, v168
	s_cbranch_vccz .LBB0_1419
	s_and_saveexec_b64 s[0:1], s[2:3]
	ds_write_b32 v177, v168 offset:128
	s_or_b64 exec, exec, s[0:1]
	s_waitcnt lgkmcnt(0)
	v_add_u32_e32 v139, v159, v156
	ds_read_b128 v[140:143], v139 offset:224
	ds_read_b128 v[144:147], v139 offset:192
	ds_read_b128 v[148:151], v139 offset:160
	ds_read_b128 v[172:175], v139 offset:128
	s_waitcnt lgkmcnt(0)
	v_pk_mul_f32 v[14:15], v[14:15], v[140:141]
	v_pk_mul_f32 v[10:11], v[10:11], v[144:145]
	v_pk_mul_f32 v[6:7], v[6:7], v[148:149]
	v_pk_mul_f32 v[16:17], v[16:17], v[142:143]
	v_pk_mul_f32 v[12:13], v[12:13], v[146:147]
	v_pk_mul_f32 v[8:9], v[8:9], v[150:151]
	v_pk_mul_f32 v[4:5], v[4:5], v[174:175]
	v_pk_mul_f32 v[2:3], v[2:3], v[172:173]
	v_pk_mul_f32 v[62:63], v[62:63], v[140:141]
	v_pk_mul_f32 v[58:59], v[58:59], v[144:145]
	v_pk_mul_f32 v[54:55], v[54:55], v[148:149]
	v_pk_mul_f32 v[64:65], v[64:65], v[142:143]
	v_pk_mul_f32 v[60:61], v[60:61], v[146:147]
	v_pk_mul_f32 v[56:57], v[56:57], v[150:151]
	v_pk_mul_f32 v[52:53], v[52:53], v[174:175]
	v_pk_mul_f32 v[50:51], v[50:51], v[172:173]
	v_pk_mul_f32 v[46:47], v[46:47], v[140:141]
	v_pk_mul_f32 v[42:43], v[42:43], v[144:145]
	v_pk_mul_f32 v[38:39], v[38:39], v[148:149]
	v_pk_mul_f32 v[48:49], v[48:49], v[142:143]
	v_pk_mul_f32 v[44:45], v[44:45], v[146:147]
	v_pk_mul_f32 v[40:41], v[40:41], v[150:151]
	v_pk_mul_f32 v[36:37], v[36:37], v[174:175]
	v_pk_mul_f32 v[34:35], v[34:35], v[172:173]
	v_pk_mul_f32 v[30:31], v[30:31], v[140:141]
	v_pk_mul_f32 v[26:27], v[26:27], v[144:145]
	v_pk_mul_f32 v[22:23], v[22:23], v[148:149]
	v_pk_mul_f32 v[32:33], v[32:33], v[142:143]
	v_pk_mul_f32 v[28:29], v[28:29], v[146:147]
	v_pk_mul_f32 v[24:25], v[24:25], v[150:151]
	v_pk_mul_f32 v[20:21], v[20:21], v[174:175]
	v_pk_mul_f32 v[18:19], v[18:19], v[172:173]
